# v3_pk
# baseline (speedup 1.0000x reference)
.LBB3_46:
	v_cmp_eq_u32_e32 vcc, 2, v3
	s_mov_b64 s[4:5], -1
	s_and_saveexec_b64 s[44:45], vcc
	s_cbranch_execz .LBB3_56
	v_lshrrev_b32_e32 v2, 2, v2
	v_and_b32_e32 v22, 12, v2
	v_mul_u32_u24_e32 v4, 48, v105
	v_or_b32_e32 v3, v22, v4
	v_lshlrev_b32_e32 v5, 2, v3
	v_or_b32_e32 v24, 3, v2
	v_or_b32_e32 v69, 19, v2
	v_or_b32_e32 v2, 35, v2
	v_or_b32_e32 v3, v24, v4
	v_add_lshl_u32 v26, v69, v4, 2
	v_add_lshl_u32 v4, v2, v4, 2
	v_add_u32_e32 v27, 0xc00, v5
	s_waitcnt lgkmcnt(0)
	global_load_dwordx3 v[6:8], v5, s[12:13]
	global_load_dwordx3 v[10:12], v5, s[14:15]
	v_lshlrev_b32_e32 v25, 2, v3
	global_load_dwordx3 v[14:16], v5, s[12:13] offset:64
	global_load_dwordx3 v[18:20], v5, s[14:15] offset:64
	global_load_dword v3, v25, s[12:13]
	global_load_dword v9, v25, s[14:15]
	global_load_dwordx3 v[32:34], v5, s[12:13] offset:128
	global_load_dwordx3 v[36:38], v5, s[14:15] offset:128
	global_load_dword v13, v26, s[12:13]
	global_load_dword v17, v26, s[14:15]
	global_load_dword v21, v4, s[12:13]
	global_load_dword v23, v4, s[14:15]
	global_load_dwordx3 v[40:42], v27, s[12:13] offset:64
	global_load_dwordx3 v[44:46], v27, s[14:15] offset:64
	global_load_dword v35, v26, s[12:13] offset:3072
	global_load_dword v39, v26, s[14:15] offset:3072
	global_load_dwordx3 v[48:50], v27, s[12:13] offset:128
	global_load_dwordx3 v[52:54], v27, s[14:15] offset:128
	v_mov_b32_e32 v26, 0x600
	v_mad_u32_u24 v73, v105, 48, v26
	global_load_dword v43, v4, s[12:13] offset:3072
	global_load_dword v47, v4, s[14:15] offset:3072
	global_load_dwordx2 v[74:75], v5, s[12:13] offset:3072
	global_load_dwordx2 v[76:77], v5, s[14:15] offset:3072
	global_load_dword v79, v25, s[12:13] offset:3072
	global_load_dword v81, v25, s[14:15] offset:3072
	global_load_dword v78, v27, s[12:13] offset:8
	global_load_dword v80, v27, s[14:15] offset:8
	v_or_b32_e32 v4, v22, v73
	v_lshlrev_b32_e32 v4, 2, v4
	v_add_lshl_u32 v2, v2, v73, 2
	global_load_dwordx3 v[56:58], v4, s[12:13] offset:128
	global_load_dwordx3 v[60:62], v4, s[14:15] offset:128
	global_load_dword v51, v2, s[12:13]
	global_load_dword v55, v2, s[14:15]
	global_load_dwordx3 v[66:68], v4, s[12:13]
	global_load_dwordx3 v[70:72], v4, s[14:15]
	v_or_b32_e32 v2, v24, v73
	v_lshlrev_b32_e32 v2, 2, v2
	global_load_dword v59, v2, s[12:13]
	global_load_dword v63, v2, s[14:15]
	global_load_dwordx3 v[28:30], v4, s[12:13] offset:64
	global_load_dwordx3 v[24:26], v4, s[14:15] offset:64
	v_lshl_or_b32 v31, v64, 4, v22
	v_cmp_eq_u32_e64 s[4:5], 3, v64
	s_mov_b32 s6, 0x4038aa3b
	s_mov_b32 s3, 0x3fb8aa3b
	v_cndmask_b32_e64 v2, v31, 0, s[4:5]
	v_lshlrev_b32_e32 v2, 2, v2
	global_load_dword v27, v2, s[24:25]
	s_mov_b32 s33, 0x3f2aaaab
	v_mov_b32_e32 v4, 0
	v_mov_b32_e32 v5, v4
	s_waitcnt vmcnt(36)
	v_mov_b32_e32 v2, v8
	s_waitcnt vmcnt(35)
	v_pk_mul_f32 v[6:7], v[6:7], v[10:11]
	v_mov_b32_e32 v8, v12
	s_waitcnt vmcnt(33)
	v_pk_mul_f32 v[10:11], v[14:15], v[18:19]
	v_mov_b32_e32 v12, v16
	v_mov_b32_e32 v16, v20
	s_waitcnt vmcnt(29)
	v_pk_mul_f32 v[14:15], v[32:33], v[36:37]
	v_mov_b32_e32 v20, v34
	v_mov_b32_e32 v22, v38
	v_pk_mul_f32 v[2:3], v[2:3], v[8:9]
	v_pk_mul_f32 v[8:9], v[10:11], s[6:7] op_sel_hi:[1,0]
	s_waitcnt vmcnt(27)
	v_pk_mul_f32 v[10:11], v[12:13], v[16:17]
	v_pk_mul_f32 v[12:13], v[14:15], s[6:7] op_sel_hi:[1,0]
	s_waitcnt vmcnt(25)
	v_pk_mul_f32 v[14:15], v[20:21], v[22:23]
	v_pk_mul_f32 v[16:17], v[2:3], s[6:7] op_sel_hi:[1,0]
	v_pk_mul_f32 v[10:11], v[10:11], s[6:7] op_sel_hi:[1,0]
	v_cvt_pk_f16_f32 v2, v12, v13
	v_pk_mul_f32 v[12:13], v[14:15], s[6:7] op_sel_hi:[1,0]
	s_waitcnt vmcnt(24)
	v_mov_b32_e32 v34, v42
	s_waitcnt vmcnt(23)
	v_mov_b32_e32 v38, v46
	s_waitcnt vmcnt(1)
	v_pk_mul_f32 v[24:25], v[28:29], v[24:25]
	v_or_b32_e32 v28, 1, v31
	v_cvt_pk_f16_f32 v8, v8, v9
	v_cvt_pk_f16_f32 v9, v10, v11
	v_cvt_pk_f16_f32 v3, v12, v13
	v_pk_mul_f32 v[10:11], v[40:41], v[44:45]
	v_pk_mul_f32 v[12:13], v[34:35], v[38:39]
	v_cndmask_b32_e64 v28, v28, 0, s[4:5]
	v_or_b32_e32 v29, 2, v31
	v_or_b32_e32 v31, 3, v31
	v_pk_mul_f32 v[10:11], v[10:11], s[6:7] op_sel_hi:[1,0]
	v_pk_mul_f32 v[12:13], v[12:13], s[6:7] op_sel_hi:[1,0]
	v_mov_b32_e32 v42, v50
	v_mov_b32_e32 v46, v54
	v_mov_b32_e32 v50, v58
	v_mov_b32_e32 v54, v62
	v_lshlrev_b32_e32 v28, 2, v28
	v_cndmask_b32_e64 v29, v29, 0, s[4:5]
	v_cndmask_b32_e64 v31, v31, 0, s[4:5]
	v_cvt_pk_f16_f32 v10, v10, v11
	v_cvt_pk_f16_f32 v11, v12, v13
	v_pk_mul_f32 v[12:13], v[48:49], v[52:53]
	v_pk_mul_f32 v[20:21], v[50:51], v[54:55]
	v_lshlrev_b32_e32 v29, 2, v29
	v_lshlrev_b32_e32 v31, 2, v31
	global_load_dword v50, v28, s[24:25]
	global_load_dword v52, v29, s[24:25]
	global_load_dword v54, v31, s[24:25]
	s_waitcnt vmcnt(3)
	v_mul_f32_e32 v28, 0x3fb8aa3b, v27
	v_fma_f32 v29, v27, s3, -v28
	v_rndne_f32_e32 v31, v28
	v_pk_mul_f32 v[14:15], v[42:43], v[46:47]
	v_fmac_f32_e32 v29, 0x32a5705f, v27
	v_sub_f32_e32 v28, v28, v31
	v_pk_mul_f32 v[12:13], v[12:13], s[6:7] op_sel_hi:[1,0]
	v_pk_mul_f32 v[14:15], v[14:15], s[6:7] op_sel_hi:[1,0]
	v_add_f32_e32 v28, v28, v29
	v_cvt_pk_f16_f32 v12, v12, v13
	v_cvt_pk_f16_f32 v13, v14, v15
	v_pk_mul_f32 v[14:15], v[74:75], v[76:77]
	v_exp_f32_e32 v28, v28
	v_cvt_i32_f32_e32 v29, v31
	v_pk_mul_f32 v[6:7], v[6:7], s[6:7] op_sel_hi:[1,0]
	v_pk_mul_f32 v[14:15], v[14:15], s[6:7] op_sel_hi:[1,0]
	v_mov_b32_e32 v58, v68
	v_mov_b32_e32 v62, v72
	v_cvt_pk_f16_f32 v6, v6, v7
	v_cvt_pk_f16_f32 v7, v16, v17
	v_cvt_pk_f16_f32 v16, v14, v15
	v_pk_mul_f32 v[14:15], v[78:79], v[80:81]
	v_pk_mul_f32 v[18:19], v[56:57], v[60:61]
	v_pk_mul_f32 v[22:23], v[66:67], v[70:71]
	v_pk_mul_f32 v[32:33], v[58:59], v[62:63]
	v_pk_mul_f32 v[24:25], v[24:25], s[6:7] op_sel_hi:[1,0]
	v_pk_mul_f32 v[14:15], v[14:15], s[6:7] op_sel_hi:[1,0]
	v_pk_mul_f32 v[18:19], v[18:19], s[6:7] op_sel_hi:[1,0]
	v_pk_mul_f32 v[20:21], v[20:21], s[6:7] op_sel_hi:[1,0]
	v_pk_mul_f32 v[22:23], v[22:23], s[6:7] op_sel_hi:[1,0]
	v_pk_mul_f32 v[32:33], v[32:33], s[6:7] op_sel_hi:[1,0]
	v_cvt_pk_f16_f32 v24, v24, v25
	v_add_lshl_u32 v25, v69, v73, 2
	s_mov_b32 s7, 0xc2ce8ed0
	v_cvt_pk_f16_f32 v22, v22, v23
	v_cvt_pk_f16_f32 v23, v32, v33
	global_load_dword v33, v25, s[12:13]
	global_load_dword v35, v25, s[14:15]
	v_ldexp_f32 v25, v28, v29
	v_cmp_ngt_f32_e32 vcc, s7, v27
	s_mov_b32 s12, 0x42b17218
	v_mov_b32_e32 v32, v30
	v_cndmask_b32_e32 v25, 0, v25, vcc
	v_mov_b32_e32 v30, 0x7f800000
	v_cmp_nlt_f32_e32 vcc, s12, v27
	v_mov_b32_e32 v55, 0x3ecc95a3
	s_mov_b32 s25, 0x3f317218
	v_cndmask_b32_e32 v25, v30, v25, vcc
	v_add_f32_e32 v27, 1.0, v25
	v_add_f32_e32 v28, -1.0, v27
	v_sub_f32_e32 v29, v28, v27
	v_add_f32_e32 v29, 1.0, v29
	v_sub_f32_e32 v28, v25, v28
	v_add_f32_e32 v31, v28, v29
	v_frexp_mant_f32_e32 v34, v27
	v_cvt_f64_f32_e32 v[28:29], v27
	v_frexp_exp_i32_f64_e32 v28, v[28:29]
	v_cmp_gt_f32_e32 vcc, s33, v34
	s_mov_b32 s13, 0x7f800000
	s_mov_b32 s15, 0x33800000
	v_subbrev_co_u32_e32 v34, vcc, 0, v28, vcc
	v_sub_u32_e32 v28, 0, v34
	v_ldexp_f32 v27, v27, v28
	v_ldexp_f32 v28, v31, v28
	v_add_f32_e32 v31, -1.0, v27
	v_add_f32_e32 v29, 1.0, v31
	v_sub_f32_e32 v29, v27, v29
	v_add_f32_e32 v36, v28, v29
	v_add_f32_e32 v29, 1.0, v27
	v_add_f32_e32 v37, -1.0, v29
	v_sub_f32_e32 v27, v27, v37
	v_add_f32_e32 v27, v28, v27
	v_add_f32_e32 v42, v29, v27
	v_rcp_f32_e32 v43, v42
	v_sub_f32_e32 v28, v29, v42
	v_add_f32_e32 v29, v31, v36
	v_add_f32_e32 v27, v27, v28
	v_sub_f32_e32 v28, v31, v29
	v_mul_f32_e32 v44, v29, v43
	v_add_f32_e32 v31, v36, v28
	v_mul_f32_e32 v36, v42, v44
	v_fma_f32 v38, v44, v42, -v36
	v_fmac_f32_e32 v38, v44, v27
	v_add_f32_e32 v28, v36, v38
	v_sub_f32_e32 v37, v29, v28
	v_pk_add_f32 v[40:41], v[28:29], v[36:37] neg_lo:[0,1] neg_hi:[0,1]
	v_mov_b32_e32 v39, v28
	v_pk_add_f32 v[28:29], v[40:41], v[38:39] neg_lo:[0,1] neg_hi:[0,1]
	v_cmp_neq_f32_e32 vcc, s13, v25
	v_add_f32_e32 v29, v31, v29
	v_add_f32_e32 v28, v28, v29
	v_add_f32_e32 v29, v37, v28
	v_mul_f32_e32 v31, v43, v29
	v_mul_f32_e32 v36, v42, v31
	v_fma_f32 v38, v31, v42, -v36
	v_fmac_f32_e32 v38, v31, v27
	v_sub_f32_e32 v27, v37, v29
	v_add_f32_e32 v27, v28, v27
	v_add_f32_e32 v28, v36, v38
	v_sub_f32_e32 v37, v29, v28
	v_pk_add_f32 v[40:41], v[28:29], v[36:37] neg_lo:[0,1] neg_hi:[0,1]
	v_mov_b32_e32 v39, v28
	v_pk_add_f32 v[28:29], v[40:41], v[38:39] neg_lo:[0,1] neg_hi:[0,1]
	v_cvt_f32_i32_e32 v36, v34
	v_add_f32_e32 v27, v27, v29
	v_add_f32_e32 v27, v28, v27
	v_add_f32_e32 v28, v44, v31
	v_add_f32_e32 v27, v37, v27
	v_sub_f32_e32 v29, v28, v44
	v_mul_f32_e32 v27, v43, v27
	v_sub_f32_e32 v29, v31, v29
	v_add_f32_e32 v27, v29, v27
	v_add_f32_e32 v31, v28, v27
	v_mul_f32_e32 v37, v31, v31
	v_fmamk_f32 v29, v37, 0x3e9b6dac, v55
	v_sub_f32_e32 v28, v31, v28
	v_fmaak_f32 v29, v37, v29, 0x3f2aaada
	v_sub_f32_e32 v27, v27, v28
	v_mul_f32_e32 v37, v31, v37
	v_mov_b32_e32 v28, 0x3f317218
	v_pk_mul_f32 v[40:41], v[36:37], v[28:29]
	v_ldexp_f32 v39, v31, 1
	v_fma_f32 v38, v36, s25, -v40
	v_fmac_f32_e32 v38, 0xb102e308, v36
	v_pk_add_f32 v[36:37], v[40:41], v[38:39]
	v_ldexp_f32 v27, v27, 1
	v_sub_f32_e32 v29, v37, v39
	v_sub_f32_e32 v29, v41, v29
	v_add_f32_e32 v43, v27, v29
	v_mov_b32_e32 v42, v40
	v_pk_add_f32 v[40:41], v[36:37], v[40:41] neg_lo:[0,1] neg_hi:[0,1]
	v_pk_add_f32 v[44:45], v[36:37], v[42:43]
	v_mov_b32_e32 v39, v36
	v_mov_b32_e32 v41, v45
	v_pk_add_f32 v[46:47], v[38:39], v[40:41] neg_lo:[0,1] neg_hi:[0,1]
	v_pk_add_f32 v[38:39], v[38:39], v[40:41]
	v_mov_b32_e32 v42, v43
	v_pk_add_f32 v[40:41], v[38:39], v[36:37] op_sel:[1,0] op_sel_hi:[0,1] neg_lo:[0,1] neg_hi:[0,1]
	v_pk_add_f32 v[48:49], v[44:45], v[40:41] op_sel_hi:[1,0] neg_lo:[0,1] neg_hi:[0,1]
	v_mov_b32_e32 v44, v45
	v_mov_b32_e32 v45, v39
	v_pk_mov_b32 v[40:41], v[36:37], v[40:41] op_sel:[1,0]
	v_mov_b32_e32 v43, v36
	v_pk_add_f32 v[40:41], v[44:45], v[40:41] neg_lo:[0,1] neg_hi:[0,1]
	v_mov_b32_e32 v48, v46
	v_pk_add_f32 v[36:37], v[42:43], v[40:41] neg_lo:[0,1] neg_hi:[0,1]
	v_mov_b32_e32 v47, v39
	v_pk_add_f32 v[40:41], v[48:49], v[36:37]
	s_mov_b32 s24, 0x3c23d70a
	v_pk_add_f32 v[42:43], v[40:41], v[40:41] op_sel:[0,1] op_sel_hi:[1,0]
	v_mov_b32_e32 v31, 0x41200000
	v_pk_add_f32 v[38:39], v[38:39], v[42:43] op_sel:[1,0] op_sel_hi:[0,1]
	v_mov_b32_e32 v41, v38
	v_pk_add_f32 v[44:45], v[40:41], v[46:47] neg_lo:[0,1] neg_hi:[0,1]
	v_mov_b32_e32 v37, v42
	v_sub_f32_e32 v27, v40, v44
	v_pk_add_f32 v[36:37], v[36:37], v[44:45] neg_lo:[0,1] neg_hi:[0,1]
	v_sub_f32_e32 v27, v46, v27
	v_add_f32_e32 v27, v36, v27
	v_add_f32_e32 v27, v27, v37
	v_add_f32_e32 v27, v38, v27
	v_cndmask_b32_e32 v27, v30, v27, vcc
	v_cmp_lt_f32_e64 vcc, |v25|, s15
	s_mov_b32 s14, 0xbd23d70a
	v_mov_b32_e32 v34, v26
	v_cndmask_b32_e32 v25, v27, v25, vcc
	v_add_f32_e32 v25, 0x358637bd, v25
	v_med3_f32 v25, v25, s24, v31
	v_div_scale_f32 v29, s[46:47], v25, v25, s14
	v_rcp_f32_e32 v36, v29
	s_waitcnt vmcnt(0)
	v_pk_mul_f32 v[26:27], v[32:33], v[34:35]
	v_mov_b32_e32 v49, 0x3f2aaada
	v_pk_mul_f32 v[26:27], v[26:27], s[6:7] op_sel_hi:[1,0]
	v_fma_f32 v32, -v29, v36, 1.0
	v_fmac_f32_e32 v36, v32, v36
	v_div_scale_f32 v32, vcc, s14, v25, s14
	v_mul_f32_e32 v33, v32, v36
	v_fma_f32 v34, -v29, v33, v32
	v_fmac_f32_e32 v33, v34, v36
	v_fma_f32 v29, -v29, v33, v32
	v_div_fmas_f32 v29, v29, v36, v33
	v_mul_f32_e32 v33, 0x3fb8aa3b, v50
	v_fma_f32 v34, v50, s3, -v33
	v_rndne_f32_e32 v35, v33
	v_fmac_f32_e32 v34, 0x32a5705f, v50
	v_sub_f32_e32 v33, v33, v35
	v_div_fixup_f32 v46, v29, v25, s14
	v_add_f32_e32 v33, v33, v34
	v_mul_f32_e32 v25, 0x3fb8aa3b, v46
	v_exp_f32_e32 v33, v33
	v_cvt_i32_f32_e32 v34, v35
	v_fma_f32 v29, v46, s3, -v25
	v_rndne_f32_e32 v32, v25
	v_fmac_f32_e32 v29, 0x32a5705f, v46
	v_sub_f32_e32 v25, v25, v32
	v_add_f32_e32 v25, v25, v29
	v_exp_f32_e32 v47, v25
	v_ldexp_f32 v25, v33, v34
	v_cmp_ngt_f32_e32 vcc, s7, v50
	v_cvt_i32_f32_e32 v48, v32
	v_cvt_pk_f16_f32 v17, v14, v15
	v_cndmask_b32_e32 v25, 0, v25, vcc
	v_cmp_nlt_f32_e32 vcc, s12, v50
	v_mov_b32_e32 v14, v4
	v_mov_b32_e32 v15, v4
	v_cndmask_b32_e32 v25, v30, v25, vcc
	v_add_f32_e32 v29, 1.0, v25
	v_add_f32_e32 v32, -1.0, v29
	v_sub_f32_e32 v33, v32, v29
	v_add_f32_e32 v33, 1.0, v33
	v_sub_f32_e32 v32, v25, v32
	v_add_f32_e32 v34, v32, v33
	v_frexp_mant_f32_e32 v35, v29
	v_cvt_f64_f32_e32 v[32:33], v29
	v_frexp_exp_i32_f64_e32 v32, v[32:33]
	v_cmp_gt_f32_e32 vcc, s33, v35
	v_cvt_pk_f16_f32 v18, v18, v19
	v_cvt_pk_f16_f32 v19, v20, v21
	v_subbrev_co_u32_e32 v40, vcc, 0, v32, vcc
	v_sub_u32_e32 v32, 0, v40
	v_ldexp_f32 v29, v29, v32
	v_ldexp_f32 v32, v34, v32
	v_add_f32_e32 v34, -1.0, v29
	v_add_f32_e32 v33, 1.0, v34
	v_sub_f32_e32 v33, v29, v33
	v_add_f32_e32 v35, v32, v33
	v_add_f32_e32 v33, 1.0, v29
	v_add_f32_e32 v36, -1.0, v33
	v_sub_f32_e32 v29, v29, v36
	v_add_f32_e32 v29, v32, v29
	v_add_f32_e32 v41, v33, v29
	v_rcp_f32_e32 v42, v41
	v_sub_f32_e32 v32, v33, v41
	v_add_f32_e32 v33, v34, v35
	v_add_f32_e32 v29, v29, v32
	v_mul_f32_e32 v44, v33, v42
	v_sub_f32_e32 v32, v34, v33
	v_mul_f32_e32 v34, v41, v44
	v_fma_f32 v36, v44, v41, -v34
	v_fmac_f32_e32 v36, v44, v29
	v_add_f32_e32 v43, v35, v32
	v_add_f32_e32 v32, v34, v36
	v_sub_f32_e32 v35, v33, v32
	v_pk_add_f32 v[38:39], v[32:33], v[34:35] neg_lo:[0,1] neg_hi:[0,1]
	v_mov_b32_e32 v37, v32
	v_pk_add_f32 v[32:33], v[38:39], v[36:37] neg_lo:[0,1] neg_hi:[0,1]
	v_cmp_neq_f32_e32 vcc, s13, v25
	v_add_f32_e32 v33, v43, v33
	v_add_f32_e32 v32, v32, v33
	v_add_f32_e32 v33, v35, v32
	v_mul_f32_e32 v43, v42, v33
	v_mul_f32_e32 v34, v41, v43
	v_fma_f32 v36, v43, v41, -v34
	v_fmac_f32_e32 v36, v43, v29
	v_sub_f32_e32 v29, v35, v33
	v_add_f32_e32 v29, v32, v29
	v_add_f32_e32 v32, v34, v36
	v_sub_f32_e32 v35, v33, v32
	v_pk_add_f32 v[38:39], v[32:33], v[34:35] neg_lo:[0,1] neg_hi:[0,1]
	v_mov_b32_e32 v37, v32
	v_pk_add_f32 v[32:33], v[38:39], v[36:37] neg_lo:[0,1] neg_hi:[0,1]
	v_mov_b32_e32 v20, v4
	v_add_f32_e32 v29, v29, v33
	v_add_f32_e32 v29, v32, v29
	v_add_f32_e32 v33, v44, v43
	v_add_f32_e32 v29, v35, v29
	v_sub_f32_e32 v32, v33, v44
	v_mul_f32_e32 v29, v42, v29
	v_sub_f32_e32 v32, v43, v32
	v_add_f32_e32 v34, v32, v29
	v_add_f32_e32 v36, v33, v34
	v_cvt_f32_i32_e32 v32, v40
	v_mul_f32_e32 v37, v36, v36
	v_sub_f32_e32 v33, v36, v33
	v_fmamk_f32 v29, v37, 0x3e9b6dac, v55
	v_sub_f32_e32 v33, v34, v33
	v_fmaak_f32 v29, v37, v29, 0x3f2aaada
	v_ldexp_f32 v38, v33, 1
	v_mul_f32_e32 v33, v36, v37
	v_ldexp_f32 v35, v36, 1
	v_pk_mul_f32 v[36:37], v[32:33], v[28:29]
	v_mov_b32_e32 v21, v4
	v_fma_f32 v34, v32, s25, -v36
	v_fmac_f32_e32 v34, 0xb102e308, v32
	v_pk_add_f32 v[32:33], v[36:37], v[34:35]
	s_nop 0
	v_sub_f32_e32 v29, v33, v35
	v_sub_f32_e32 v29, v37, v29
	v_add_f32_e32 v39, v38, v29
	v_mov_b32_e32 v38, v36
	v_pk_add_f32 v[36:37], v[32:33], v[36:37] neg_lo:[0,1] neg_hi:[0,1]
	v_pk_add_f32 v[40:41], v[32:33], v[38:39]
	v_mov_b32_e32 v35, v32
	v_mov_b32_e32 v37, v41
	v_pk_add_f32 v[42:43], v[34:35], v[36:37] neg_lo:[0,1] neg_hi:[0,1]
	v_pk_add_f32 v[34:35], v[34:35], v[36:37]
	v_mov_b32_e32 v38, v39
	v_pk_add_f32 v[36:37], v[34:35], v[32:33] op_sel:[1,0] op_sel_hi:[0,1] neg_lo:[0,1] neg_hi:[0,1]
	v_pk_add_f32 v[44:45], v[40:41], v[36:37] op_sel_hi:[1,0] neg_lo:[0,1] neg_hi:[0,1]
	v_mov_b32_e32 v40, v41
	v_mov_b32_e32 v41, v35
	v_pk_mov_b32 v[36:37], v[32:33], v[36:37] op_sel:[1,0]
	v_mov_b32_e32 v39, v32
	v_pk_add_f32 v[36:37], v[40:41], v[36:37] neg_lo:[0,1] neg_hi:[0,1]
	v_mov_b32_e32 v44, v42
	v_pk_add_f32 v[32:33], v[38:39], v[36:37] neg_lo:[0,1] neg_hi:[0,1]
	v_mov_b32_e32 v43, v35
	v_pk_add_f32 v[36:37], v[44:45], v[32:33]
	s_nop 0
	v_pk_add_f32 v[38:39], v[36:37], v[36:37] op_sel:[0,1] op_sel_hi:[1,0]
	s_nop 0
	v_pk_add_f32 v[34:35], v[34:35], v[38:39] op_sel:[1,0] op_sel_hi:[0,1]
	v_mov_b32_e32 v37, v34
	v_pk_add_f32 v[40:41], v[36:37], v[42:43] neg_lo:[0,1] neg_hi:[0,1]
	v_mov_b32_e32 v33, v38
	v_sub_f32_e32 v29, v36, v40
	v_pk_add_f32 v[32:33], v[32:33], v[40:41] neg_lo:[0,1] neg_hi:[0,1]
	v_sub_f32_e32 v29, v42, v29
	v_add_f32_e32 v29, v32, v29
	v_add_f32_e32 v29, v29, v33
	v_add_f32_e32 v29, v34, v29
	v_cndmask_b32_e32 v29, v30, v29, vcc
	v_cmp_lt_f32_e64 vcc, |v25|, s15
	s_nop 1
	v_cndmask_b32_e32 v25, v29, v25, vcc
	v_add_f32_e32 v25, 0x358637bd, v25
	v_med3_f32 v29, v25, s24, v31
	v_div_scale_f32 v32, s[46:47], v29, v29, s14
	v_rcp_f32_e32 v33, v32
	v_cvt_pk_f16_f32 v25, v26, v27
	v_ldexp_f32 v26, v47, v48
	v_fma_f32 v27, -v32, v33, 1.0
	v_fmac_f32_e32 v33, v27, v33
	v_div_scale_f32 v27, vcc, s14, v29, s14
	v_mul_f32_e32 v34, v27, v33
	v_fma_f32 v35, -v32, v34, v27
	v_fmac_f32_e32 v34, v35, v33
	v_fma_f32 v27, -v32, v34, v27
	v_div_fmas_f32 v27, v27, v33, v34
	v_div_fixup_f32 v27, v27, v29, s14
	v_mul_f32_e32 v29, 0x3fb8aa3b, v27
	v_fma_f32 v32, v27, s3, -v29
	v_rndne_f32_e32 v33, v29
	v_fmac_f32_e32 v32, 0x32a5705f, v27
	v_sub_f32_e32 v29, v29, v33
	v_add_f32_e32 v29, v29, v32
	v_exp_f32_e32 v29, v29
	v_cvt_i32_f32_e32 v32, v33
	v_cmp_ngt_f32_e32 vcc, s7, v46
	v_ldexp_f32 v29, v29, v32
	s_nop 0
	v_cndmask_b32_e32 v26, 0, v26, vcc
	v_cmp_nlt_f32_e32 vcc, s12, v46
	s_nop 1
	v_cndmask_b32_e32 v26, v30, v26, vcc
	v_cmp_ngt_f32_e32 vcc, s7, v27
	v_cndmask_b32_e64 v50, v26, 0, s[4:5]
	s_nop 0
	v_cndmask_b32_e32 v29, 0, v29, vcc
	v_cmp_nlt_f32_e32 vcc, s12, v27
	s_nop 1
	v_cndmask_b32_e32 v27, v30, v29, vcc
	v_mul_f32_e32 v29, 0x3fb8aa3b, v52
	v_fma_f32 v32, v52, s3, -v29
	v_rndne_f32_e32 v33, v29
	v_fmac_f32_e32 v32, 0x32a5705f, v52
	v_sub_f32_e32 v29, v29, v33
	v_add_f32_e32 v29, v29, v32
	v_exp_f32_e32 v29, v29
	v_cvt_i32_f32_e32 v32, v33
	v_cmp_ngt_f32_e32 vcc, s7, v52
	v_cndmask_b32_e64 v51, v27, 0, s[4:5]
	v_pk_add_f32 v[26:27], v[26:27], 1.0 op_sel_hi:[1,0] neg_lo:[1,0] neg_hi:[1,0]
	v_ldexp_f32 v29, v29, v32
	v_cndmask_b32_e32 v29, 0, v29, vcc
	v_cmp_nlt_f32_e32 vcc, s12, v52
	v_cndmask_b32_e64 v52, v26, 0, s[4:5]
	v_cndmask_b32_e64 v53, v27, 0, s[4:5]
	v_cndmask_b32_e32 v46, v30, v29, vcc
	v_add_f32_e32 v29, 1.0, v46
	v_add_f32_e32 v32, -1.0, v29
	v_sub_f32_e32 v33, v32, v29
	v_add_f32_e32 v33, 1.0, v33
	v_sub_f32_e32 v32, v46, v32
	v_add_f32_e32 v34, v32, v33
	v_frexp_mant_f32_e32 v35, v29
	v_cvt_f64_f32_e32 v[32:33], v29
	v_frexp_exp_i32_f64_e32 v32, v[32:33]
	v_cmp_gt_f32_e32 vcc, s33, v35
	s_nop 1
	v_subbrev_co_u32_e32 v40, vcc, 0, v32, vcc
	v_sub_u32_e32 v32, 0, v40
	v_ldexp_f32 v29, v29, v32
	v_ldexp_f32 v32, v34, v32
	v_add_f32_e32 v34, -1.0, v29
	v_add_f32_e32 v33, 1.0, v34
	v_sub_f32_e32 v33, v29, v33
	v_add_f32_e32 v35, v32, v33
	v_add_f32_e32 v33, 1.0, v29
	v_add_f32_e32 v36, -1.0, v33
	v_sub_f32_e32 v29, v29, v36
	v_add_f32_e32 v29, v32, v29
	v_add_f32_e32 v41, v33, v29
	v_rcp_f32_e32 v42, v41
	v_sub_f32_e32 v32, v33, v41
	v_add_f32_e32 v33, v34, v35
	v_add_f32_e32 v29, v29, v32
	v_mul_f32_e32 v44, v33, v42
	v_sub_f32_e32 v32, v34, v33
	v_mul_f32_e32 v34, v41, v44
	v_fma_f32 v36, v44, v41, -v34
	v_fmac_f32_e32 v36, v44, v29
	v_add_f32_e32 v43, v35, v32
	v_add_f32_e32 v32, v34, v36
	v_sub_f32_e32 v35, v33, v32
	v_pk_add_f32 v[38:39], v[32:33], v[34:35] neg_lo:[0,1] neg_hi:[0,1]
	v_mov_b32_e32 v37, v32
	v_pk_add_f32 v[32:33], v[38:39], v[36:37] neg_lo:[0,1] neg_hi:[0,1]
	v_cmp_neq_f32_e32 vcc, s13, v46
	v_add_f32_e32 v33, v43, v33
	v_add_f32_e32 v32, v32, v33
	v_add_f32_e32 v33, v35, v32
	v_mul_f32_e32 v43, v42, v33
	v_mul_f32_e32 v34, v41, v43
	v_fma_f32 v36, v43, v41, -v34
	v_fmac_f32_e32 v36, v43, v29
	v_sub_f32_e32 v29, v35, v33
	v_add_f32_e32 v29, v32, v29
	v_add_f32_e32 v32, v34, v36
	v_sub_f32_e32 v35, v33, v32
	v_pk_add_f32 v[38:39], v[32:33], v[34:35] neg_lo:[0,1] neg_hi:[0,1]
	v_mov_b32_e32 v37, v32
	v_pk_add_f32 v[32:33], v[38:39], v[36:37] neg_lo:[0,1] neg_hi:[0,1]
	s_nop 0
	v_add_f32_e32 v29, v29, v33
	v_add_f32_e32 v29, v32, v29
	v_add_f32_e32 v33, v44, v43
	v_add_f32_e32 v29, v35, v29
	v_sub_f32_e32 v32, v33, v44
	v_mul_f32_e32 v29, v42, v29
	v_sub_f32_e32 v32, v43, v32
	v_add_f32_e32 v34, v32, v29
	v_add_f32_e32 v36, v33, v34
	v_cvt_f32_i32_e32 v32, v40
	v_mul_f32_e32 v37, v36, v36
	v_sub_f32_e32 v33, v36, v33
	v_fmamk_f32 v29, v37, 0x3e9b6dac, v55
	v_sub_f32_e32 v33, v34, v33
	v_fmaak_f32 v29, v37, v29, 0x3f2aaada
	v_ldexp_f32 v38, v33, 1
	v_mul_f32_e32 v33, v36, v37
	v_ldexp_f32 v35, v36, 1
	v_pk_mul_f32 v[36:37], v[32:33], v[28:29]
	s_nop 0
	v_fma_f32 v34, v32, s25, -v36
	v_fmac_f32_e32 v34, 0xb102e308, v32
	v_pk_add_f32 v[32:33], v[36:37], v[34:35]
	s_nop 0
	v_sub_f32_e32 v29, v33, v35
	v_sub_f32_e32 v29, v37, v29
	v_add_f32_e32 v39, v38, v29
	v_mov_b32_e32 v38, v36
	v_pk_add_f32 v[36:37], v[32:33], v[36:37] neg_lo:[0,1] neg_hi:[0,1]
	v_pk_add_f32 v[40:41], v[32:33], v[38:39]
	v_mov_b32_e32 v35, v32
	v_mov_b32_e32 v37, v41
	v_pk_add_f32 v[42:43], v[34:35], v[36:37] neg_lo:[0,1] neg_hi:[0,1]
	v_pk_add_f32 v[34:35], v[34:35], v[36:37]
	v_mov_b32_e32 v38, v39
	v_pk_add_f32 v[36:37], v[34:35], v[32:33] op_sel:[1,0] op_sel_hi:[0,1] neg_lo:[0,1] neg_hi:[0,1]
	v_pk_add_f32 v[44:45], v[40:41], v[36:37] op_sel_hi:[1,0] neg_lo:[0,1] neg_hi:[0,1]
	v_mov_b32_e32 v40, v41
	v_mov_b32_e32 v41, v35
	v_pk_mov_b32 v[36:37], v[32:33], v[36:37] op_sel:[1,0]
	v_mov_b32_e32 v39, v32
	v_pk_add_f32 v[36:37], v[40:41], v[36:37] neg_lo:[0,1] neg_hi:[0,1]
	v_mov_b32_e32 v44, v42
	v_pk_add_f32 v[32:33], v[38:39], v[36:37] neg_lo:[0,1] neg_hi:[0,1]
	v_mov_b32_e32 v43, v35
	v_pk_add_f32 v[36:37], v[44:45], v[32:33]
	s_nop 0
	v_pk_add_f32 v[38:39], v[36:37], v[36:37] op_sel:[0,1] op_sel_hi:[1,0]
	s_nop 0
	v_pk_add_f32 v[34:35], v[34:35], v[38:39] op_sel:[1,0] op_sel_hi:[0,1]
	v_mov_b32_e32 v37, v34
	v_pk_add_f32 v[40:41], v[36:37], v[42:43] neg_lo:[0,1] neg_hi:[0,1]
	v_mov_b32_e32 v33, v38
	v_sub_f32_e32 v29, v36, v40
	v_pk_add_f32 v[32:33], v[32:33], v[40:41] neg_lo:[0,1] neg_hi:[0,1]
	v_sub_f32_e32 v29, v42, v29
	v_add_f32_e32 v29, v32, v29
	v_add_f32_e32 v29, v29, v33
	v_add_f32_e32 v29, v34, v29
	v_cndmask_b32_e32 v29, v30, v29, vcc
	v_cmp_lt_f32_e64 vcc, |v46|, s15
	v_pk_mul_f32 v[32:33], v[26:27], -2.0 op_sel_hi:[1,0]
	s_nop 0
	v_cndmask_b32_e32 v29, v29, v46, vcc
	v_add_f32_e32 v29, 0x358637bd, v29
	v_med3_f32 v29, v29, s24, v31
	v_div_scale_f32 v34, s[46:47], v29, v29, s14
	v_rcp_f32_e32 v35, v34
	s_nop 0
	v_fma_f32 v26, -v34, v35, 1.0
	v_fmac_f32_e32 v35, v26, v35
	v_div_scale_f32 v26, vcc, s14, v29, s14
	v_mul_f32_e32 v27, v26, v35
	v_fma_f32 v36, -v34, v27, v26
	v_fmac_f32_e32 v27, v36, v35
	v_fma_f32 v26, -v34, v27, v26
	v_mul_f32_e32 v34, 0x3fb8aa3b, v54
	v_div_fmas_f32 v26, v26, v35, v27
	v_fma_f32 v35, v54, s3, -v34
	v_rndne_f32_e32 v36, v34
	v_fmac_f32_e32 v35, 0x32a5705f, v54
	v_sub_f32_e32 v34, v34, v36
	v_div_fixup_f32 v44, v26, v29, s14
	v_add_f32_e32 v34, v34, v35
	v_mul_f32_e32 v26, 0x3fb8aa3b, v44
	v_exp_f32_e32 v34, v34
	v_cvt_i32_f32_e32 v35, v36
	v_fma_f32 v27, v44, s3, -v26
	v_rndne_f32_e32 v29, v26
	v_fmac_f32_e32 v27, 0x32a5705f, v44
	v_sub_f32_e32 v26, v26, v29
	v_add_f32_e32 v26, v26, v27
	v_exp_f32_e32 v45, v26
	v_ldexp_f32 v26, v34, v35
	v_cmp_ngt_f32_e32 vcc, s7, v54
	v_cvt_i32_f32_e32 v46, v29
	s_nop 0
	v_cndmask_b32_e32 v26, 0, v26, vcc
	v_cmp_nlt_f32_e32 vcc, s12, v54
	v_cndmask_b32_e64 v54, v32, 0, s[4:5]
	s_nop 0
	v_cndmask_b32_e32 v47, v30, v26, vcc
	v_add_f32_e32 v29, 1.0, v47
	v_add_f32_e32 v26, -1.0, v29
	v_sub_f32_e32 v27, v26, v29
	v_add_f32_e32 v27, 1.0, v27
	v_sub_f32_e32 v26, v47, v26
	v_add_f32_e32 v34, v26, v27
	v_frexp_mant_f32_e32 v35, v29
	v_cvt_f64_f32_e32 v[26:27], v29
	v_frexp_exp_i32_f64_e32 v26, v[26:27]
	v_cmp_gt_f32_e32 vcc, s33, v35
	s_nop 1
	v_subbrev_co_u32_e32 v40, vcc, 0, v26, vcc
	v_sub_u32_e32 v26, 0, v40
	v_ldexp_f32 v27, v29, v26
	v_add_f32_e32 v29, -1.0, v27
	v_add_f32_e32 v35, 1.0, v27
	v_ldexp_f32 v26, v34, v26
	v_add_f32_e32 v34, 1.0, v29
	v_add_f32_e32 v36, -1.0, v35
	v_sub_f32_e32 v34, v27, v34
	v_sub_f32_e32 v27, v27, v36
	v_add_f32_e32 v34, v26, v34
	v_add_f32_e32 v26, v26, v27
	v_add_f32_e32 v41, v35, v26
	v_rcp_f32_e32 v43, v41
	v_sub_f32_e32 v27, v35, v41
	v_add_f32_e32 v42, v26, v27
	v_add_f32_e32 v27, v29, v34
	v_sub_f32_e32 v26, v29, v27
	v_mul_f32_e32 v48, v27, v43
	v_add_f32_e32 v29, v34, v26
	v_mul_f32_e32 v34, v41, v48
	v_fma_f32 v36, v48, v41, -v34
	v_fmac_f32_e32 v36, v48, v42
	v_add_f32_e32 v26, v34, v36
	v_sub_f32_e32 v35, v27, v26
	v_pk_add_f32 v[38:39], v[26:27], v[34:35] neg_lo:[0,1] neg_hi:[0,1]
	v_mov_b32_e32 v37, v26
	v_pk_add_f32 v[26:27], v[38:39], v[36:37] neg_lo:[0,1] neg_hi:[0,1]
	v_cmp_neq_f32_e32 vcc, s13, v47
	v_add_f32_e32 v27, v29, v27
	v_add_f32_e32 v26, v26, v27
	v_add_f32_e32 v27, v35, v26
	v_mul_f32_e32 v29, v43, v27
	v_mul_f32_e32 v34, v41, v29
	v_fma_f32 v36, v29, v41, -v34
	v_fmac_f32_e32 v36, v29, v42
	v_sub_f32_e32 v35, v35, v27
	v_add_f32_e32 v41, v26, v35
	v_add_f32_e32 v26, v34, v36
	v_sub_f32_e32 v35, v27, v26
	v_pk_add_f32 v[38:39], v[26:27], v[34:35] neg_lo:[0,1] neg_hi:[0,1]
	v_mov_b32_e32 v37, v26
	v_pk_add_f32 v[26:27], v[38:39], v[36:37] neg_lo:[0,1] neg_hi:[0,1]
	s_nop 0
	v_add_f32_e32 v27, v41, v27
	v_add_f32_e32 v26, v26, v27
	v_add_f32_e32 v27, v48, v29
	v_add_f32_e32 v26, v35, v26
	v_sub_f32_e32 v34, v27, v48
	v_mul_f32_e32 v26, v43, v26
	v_sub_f32_e32 v29, v29, v34
	v_add_f32_e32 v29, v29, v26
	v_add_f32_e32 v34, v27, v29
	v_mul_f32_e32 v36, v34, v34
	v_cvt_f32_i32_e32 v26, v40
	v_fmac_f32_e32 v55, 0x3e9b6dac, v36
	v_sub_f32_e32 v27, v34, v27
	v_fmac_f32_e32 v49, v36, v55
	v_sub_f32_e32 v27, v29, v27
	v_ldexp_f32 v37, v27, 1
	v_mul_f32_e32 v27, v34, v36
	v_mov_b32_e32 v29, v49
	v_pk_mul_f32 v[28:29], v[26:27], v[28:29]
	v_ldexp_f32 v35, v34, 1
	v_fma_f32 v34, v26, s25, -v28
	v_fmac_f32_e32 v34, 0xb102e308, v26
	v_pk_add_f32 v[26:27], v[28:29], v[34:35]
	v_mov_b32_e32 v36, v28
	v_sub_f32_e32 v35, v27, v35
	v_sub_f32_e32 v35, v29, v35
	v_add_f32_e32 v37, v37, v35
	v_pk_add_f32 v[28:29], v[26:27], v[28:29] neg_lo:[0,1] neg_hi:[0,1]
	v_pk_add_f32 v[38:39], v[26:27], v[36:37]
	v_mov_b32_e32 v35, v26
	v_mov_b32_e32 v29, v39
	v_pk_add_f32 v[40:41], v[34:35], v[28:29] neg_lo:[0,1] neg_hi:[0,1]
	v_pk_add_f32 v[28:29], v[34:35], v[28:29]
	v_mov_b32_e32 v36, v37
	v_pk_add_f32 v[34:35], v[28:29], v[26:27] op_sel:[1,0] op_sel_hi:[0,1] neg_lo:[0,1] neg_hi:[0,1]
	v_pk_add_f32 v[42:43], v[38:39], v[34:35] op_sel_hi:[1,0] neg_lo:[0,1] neg_hi:[0,1]
	v_mov_b32_e32 v38, v39
	v_mov_b32_e32 v39, v29
	v_pk_mov_b32 v[34:35], v[26:27], v[34:35] op_sel:[1,0]
	v_mov_b32_e32 v37, v26
	v_pk_add_f32 v[34:35], v[38:39], v[34:35] neg_lo:[0,1] neg_hi:[0,1]
	v_mov_b32_e32 v42, v40
	v_pk_add_f32 v[26:27], v[36:37], v[34:35] neg_lo:[0,1] neg_hi:[0,1]
	v_mov_b32_e32 v41, v29
	v_pk_add_f32 v[34:35], v[42:43], v[26:27]
	v_cndmask_b32_e64 v55, v33, 0, s[4:5]
	v_pk_add_f32 v[36:37], v[34:35], v[34:35] op_sel:[0,1] op_sel_hi:[1,0]
	s_nop 0
	v_pk_add_f32 v[28:29], v[28:29], v[36:37] op_sel:[1,0] op_sel_hi:[0,1]
	v_mov_b32_e32 v35, v28
	v_pk_add_f32 v[38:39], v[34:35], v[40:41] neg_lo:[0,1] neg_hi:[0,1]
	v_mov_b32_e32 v27, v36
	v_sub_f32_e32 v29, v34, v38
	v_pk_add_f32 v[26:27], v[26:27], v[38:39] neg_lo:[0,1] neg_hi:[0,1]
	v_sub_f32_e32 v29, v40, v29
	v_add_f32_e32 v26, v26, v29
	v_add_f32_e32 v26, v26, v27
	v_add_f32_e32 v26, v28, v26
	v_cndmask_b32_e32 v26, v30, v26, vcc
	v_cmp_lt_f32_e64 vcc, |v47|, s15
	v_ldexp_f32 v29, v45, v46
	s_nop 0
	v_cndmask_b32_e32 v26, v26, v47, vcc
	v_add_f32_e32 v26, 0x358637bd, v26
	v_med3_f32 v26, v26, s24, v31
	v_div_scale_f32 v27, s[24:25], v26, v26, s14
	v_rcp_f32_e32 v28, v27
	s_nop 0
	v_fma_f32 v31, -v27, v28, 1.0
	v_fmac_f32_e32 v28, v31, v28
	v_div_scale_f32 v31, vcc, s14, v26, s14
	v_mul_f32_e32 v32, v31, v28
	v_fma_f32 v33, -v27, v32, v31
	v_fmac_f32_e32 v32, v33, v28
	v_fma_f32 v27, -v27, v32, v31
	v_div_fmas_f32 v27, v27, v28, v32
	v_div_fixup_f32 v27, v27, v26, s14
	v_mul_f32_e32 v26, 0x3fb8aa3b, v27
	v_fma_f32 v28, v27, s3, -v26
	v_rndne_f32_e32 v31, v26
	v_fmac_f32_e32 v28, 0x32a5705f, v27
	v_sub_f32_e32 v26, v26, v31
	v_add_f32_e32 v26, v26, v28
	v_exp_f32_e32 v28, v26
	v_cvt_i32_f32_e32 v31, v31
	v_cmp_ngt_f32_e32 vcc, s7, v44
	s_movk_i32 s3, 0xc0
	v_mov_b32_e32 v32, v4
	v_cndmask_b32_e32 v26, 0, v29, vcc
	v_cmp_nlt_f32_e32 vcc, s12, v44
	v_ldexp_f32 v28, v28, v31
	v_mov_b32_e32 v31, v4
	v_cndmask_b32_e32 v26, v30, v26, vcc
	v_cmp_ngt_f32_e32 vcc, s7, v27
	v_cndmask_b32_e64 v56, v26, 0, s[4:5]
	v_cmp_eq_u32_e64 s[6:7], 0, v64
	v_cndmask_b32_e32 v28, 0, v28, vcc
	v_cmp_nlt_f32_e32 vcc, s12, v27
	v_mov_b32_e32 v33, v4
	s_nop 0
	v_cndmask_b32_e32 v27, v30, v28, vcc
	v_cndmask_b32_e64 v57, v27, 0, s[4:5]
	v_pk_add_f32 v[26:27], v[26:27], 1.0 op_sel_hi:[1,0] neg_lo:[1,0] neg_hi:[1,0]
	v_mov_b32_e32 v30, v4
	v_pk_mul_f32 v[28:29], v[26:27], -2.0 op_sel_hi:[1,0]
	v_cndmask_b32_e64 v59, v27, 0, s[4:5]
	v_cndmask_b32_e64 v60, v28, 0, s[4:5]
	v_lshlrev_b32_e32 v27, 6, v64
	v_mov_b32_e32 v28, 0x80
	v_cndmask_b32_e64 v27, v27, v28, s[4:5]
	v_mad_u32_u24 v27, v65, s3, v27
	v_cndmask_b32_e64 v58, v26, 0, s[4:5]
	v_mul_u32_u24_e32 v26, 0xc0, v65
	v_and_or_b32 v62, v0, 48, v27
	v_lshlrev_b32_e32 v27, 6, v65
	v_sub_u32_e32 v26, v26, v27
	v_lshl_add_u32 v26, v1, 5, v26
	v_cndmask_b32_e64 v61, v29, 0, s[4:5]
	v_lshl_or_b32 v63, v64, 3, v26
	v_cmp_gt_u32_e64 s[4:5], 2, v64
	s_mov_b32 s3, -2
	v_mov_b32_e32 v166, v6
	v_mov_b32_e32 v167, v7
	v_mov_b32_e32 v168, v8
	v_mov_b32_e32 v169, v9
	v_mov_b32_e32 v170, v2
	v_mov_b32_e32 v171, v3
	v_mov_b32_e32 v172, v4
	v_mov_b32_e32 v173, v5
	v_mov_b32_e32 v6, v166
	v_mov_b32_e32 v7, v168
	v_mov_b32_e32 v8, v170
	v_mov_b32_e32 v9, v172
	v_mov_b32_e32 v2, v167
	v_mov_b32_e32 v3, v169
	v_mov_b32_e32 v4, v171
	v_mov_b32_e32 v5, v173
	v_mov_b32_e32 v166, v10
	v_mov_b32_e32 v167, v11
	v_mov_b32_e32 v168, v12
	v_mov_b32_e32 v169, v13
	v_mov_b32_e32 v170, v14
	v_mov_b32_e32 v171, v15
	v_mov_b32_e32 v172, v16
	v_mov_b32_e32 v173, v17
	v_mov_b32_e32 v10, v166
	v_mov_b32_e32 v11, v168
	v_mov_b32_e32 v12, v170
	v_mov_b32_e32 v13, v172
	v_mov_b32_e32 v14, v167
	v_mov_b32_e32 v15, v169
	v_mov_b32_e32 v16, v171
	v_mov_b32_e32 v17, v173
	v_mov_b32_e32 v166, v18
	v_mov_b32_e32 v167, v19
	v_mov_b32_e32 v168, v20
	v_mov_b32_e32 v169, v21
	v_mov_b32_e32 v170, v22
	v_mov_b32_e32 v171, v23
	v_mov_b32_e32 v172, v24
	v_mov_b32_e32 v173, v25
	v_mov_b32_e32 v18, v166
	v_mov_b32_e32 v19, v168
	v_mov_b32_e32 v20, v170
	v_mov_b32_e32 v21, v172
	v_mov_b32_e32 v22, v167
	v_mov_b32_e32 v23, v169
	v_mov_b32_e32 v24, v171
	v_mov_b32_e32 v25, v173
	v_mov_b32_e32 v124, 0
	v_mov_b32_e32 v125, 0
	v_mov_b32_e32 v126, 0
	v_mov_b32_e32 v127, 0
	v_mov_b32_e32 v128, 0
	v_mov_b32_e32 v129, 0
	v_mov_b32_e32 v130, 0
	v_mov_b32_e32 v131, 0
	v_mov_b32_e32 v148, 0
	v_mov_b32_e32 v149, 0
	v_mov_b32_e32 v150, 0
	v_mov_b32_e32 v151, 0
	v_mov_b32_e32 v152, v52
	v_mov_b32_e32 v153, v53
	s_branch .LBB3_49
.LBB3_48:
	s_add_i32 s3, s3, 1
	s_cmpk_eq_i32 s3, 0x42
	s_waitcnt lgkmcnt(0)
	s_barrier
	s_cbranch_scc1 .LBB3_55
.LBB3_49:
	s_cmp_lt_u32 s3, 64
	s_cbranch_scc1 .Lmy_l2_main
	s_cmp_lg_u32 s3, 64
	s_cbranch_scc1 .LBB3_48
	v_mov_b32_e32 v164, v63
	v_mov_b32_e32 v165, v62
	s_nop 0
	ds_read_b128 v[64:67], v165 offset:33792
	s_waitcnt lgkmcnt(0)
	v_mfma_f32_16x16x32_f16 v[132:135], v[6:9], v[124:127], v[64:67]
	v_mfma_f32_16x16x32_f16 v[136:139], v[10:13], v[124:127], v[64:67]
	v_mfma_f32_16x16x32_f16 v[140:143], v[18:21], v[124:127], v[64:67]
	v_mfma_f32_16x16x32_f16 v[132:135], v[2:5], v[128:131], v[132:135]
	s_nop 1
	v_mfma_f32_16x16x32_f16 v[136:139], v[14:17], v[128:131], v[136:139]
	s_nop 1
	v_mfma_f32_16x16x32_f16 v[140:143], v[22:25], v[128:131], v[140:143]
	v_pk_fma_f32 v[154:155], v[56:57], v[150:151], v[58:59]
	v_pk_fma_f32 v[152:153], v[50:51], v[148:149], v[52:53]
	s_nop 2
	v_cndmask_b32_e64 v160, v136, v132, s[6:7]
	v_cndmask_b32_e64 v161, v137, v133, s[6:7]
	v_cndmask_b32_e64 v162, v138, v134, s[6:7]
	v_cndmask_b32_e64 v163, v139, v135, s[6:7]
	v_cndmask_b32_e64 v156, v140, v160, s[4:5]
	v_cndmask_b32_e64 v157, v141, v161, s[4:5]
	v_exp_f32_e32 v156, v156
	v_exp_f32_e32 v157, v157
	v_cndmask_b32_e64 v158, v142, v162, s[4:5]
	v_cndmask_b32_e64 v159, v143, v163, s[4:5]
	v_pk_add_f32 v[156:157], v[156:157], 1.0 op_sel_hi:[1,0]
	v_exp_f32_e32 v158, v158
	v_rcp_f32_e32 v156, v156
	v_rcp_f32_e32 v157, v157
	v_exp_f32_e32 v159, v159
	v_pk_fma_f32 v[148:149], v[54:55], v[156:157], v[152:153]
	v_pk_add_f32 v[158:159], v[158:159], 1.0 op_sel_hi:[1,0]
	v_cvt_pk_f16_f32 v124, v148, v149
	v_rcp_f32_e32 v158, v158
	v_rcp_f32_e32 v159, v159
	v_mov_b32_dpp v125, v124 quad_perm:[1,2,3,0] row_mask:0xf bank_mask:0xf bound_ctrl:1
	v_mov_b32_dpp v126, v124 quad_perm:[2,3,0,1] row_mask:0xf bank_mask:0xf bound_ctrl:1
	v_mov_b32_dpp v127, v124 quad_perm:[3,0,1,2] row_mask:0xf bank_mask:0xf bound_ctrl:1
	v_pk_fma_f32 v[150:151], v[60:61], v[158:159], v[154:155]
	s_nop 0
	v_cvt_pk_f16_f32 v128, v150, v151
	ds_write_b32 v164, v124 offset:16896
	s_nop 0
	v_mov_b32_dpp v129, v128 quad_perm:[1,2,3,0] row_mask:0xf bank_mask:0xf bound_ctrl:1
	v_mov_b32_dpp v130, v128 quad_perm:[2,3,0,1] row_mask:0xf bank_mask:0xf bound_ctrl:1
	v_mov_b32_dpp v131, v128 quad_perm:[3,0,1,2] row_mask:0xf bank_mask:0xf bound_ctrl:1
	ds_write_b32 v164, v128 offset:16900
	s_branch .LBB3_48
.Lmy_l2_main:
	s_and_b32 s12, s3, 1
	s_mul_i32 s13, s12, 0x3100
	s_mulk_i32 s12, 0x2100
	v_add_u32_e32 v165, s13, v62
	v_add_u32_e32 v164, s12, v63
	s_nop 0
	ds_read_b128 v[64:67], v165 offset:33792
	ds_read_b128 v[68:71], v165 offset:34576
	ds_read_b128 v[72:75], v165 offset:35360
	ds_read_b128 v[76:79], v165 offset:36144
	ds_read_b128 v[80:83], v165 offset:36928
	ds_read_b128 v[84:87], v165 offset:37712
	ds_read_b128 v[88:91], v165 offset:38496
	ds_read_b128 v[92:95], v165 offset:39280
	ds_read_b128 v[96:99], v165 offset:40064
	ds_read_b128 v[100:103], v165 offset:40848
	ds_read_b128 v[104:107], v165 offset:41632
	ds_read_b128 v[108:111], v165 offset:42416
	ds_read_b128 v[112:115], v165 offset:43200
	ds_read_b128 v[116:119], v165 offset:43984
	ds_read_b128 v[120:123], v165 offset:44768
	ds_read_b128 v[44:47], v165 offset:45552
	s_waitcnt lgkmcnt(15)
	v_mfma_f32_16x16x32_f16 v[132:135], v[6:9], v[124:127], v[64:67]
	v_mfma_f32_16x16x32_f16 v[136:139], v[10:13], v[124:127], v[64:67]
	v_mfma_f32_16x16x32_f16 v[140:143], v[18:21], v[124:127], v[64:67]
	v_mfma_f32_16x16x32_f16 v[132:135], v[2:5], v[128:131], v[132:135]
	s_nop 1
	v_mfma_f32_16x16x32_f16 v[136:139], v[14:17], v[128:131], v[136:139]
	s_nop 1
	v_mfma_f32_16x16x32_f16 v[140:143], v[22:25], v[128:131], v[140:143]
	v_pk_fma_f32 v[154:155], v[56:57], v[150:151], v[58:59]
	v_pk_fma_f32 v[152:153], v[50:51], v[148:149], v[52:53]
	s_nop 2
	v_cndmask_b32_e64 v160, v136, v132, s[6:7]
	v_cndmask_b32_e64 v161, v137, v133, s[6:7]
	v_cndmask_b32_e64 v162, v138, v134, s[6:7]
	v_cndmask_b32_e64 v163, v139, v135, s[6:7]
	v_cndmask_b32_e64 v156, v140, v160, s[4:5]
	v_cndmask_b32_e64 v157, v141, v161, s[4:5]
	v_exp_f32_e32 v156, v156
	v_exp_f32_e32 v157, v157
	v_cndmask_b32_e64 v158, v142, v162, s[4:5]
	v_cndmask_b32_e64 v159, v143, v163, s[4:5]
	v_pk_add_f32 v[156:157], v[156:157], 1.0 op_sel_hi:[1,0]
	v_exp_f32_e32 v158, v158
	v_rcp_f32_e32 v156, v156
	v_rcp_f32_e32 v157, v157
	v_exp_f32_e32 v159, v159
	v_pk_fma_f32 v[148:149], v[54:55], v[156:157], v[152:153]
	v_pk_add_f32 v[158:159], v[158:159], 1.0 op_sel_hi:[1,0]
	v_cvt_pk_f16_f32 v124, v148, v149
	v_rcp_f32_e32 v158, v158
	v_rcp_f32_e32 v159, v159
	v_mov_b32_dpp v125, v124 quad_perm:[1,2,3,0] row_mask:0xf bank_mask:0xf bound_ctrl:1
	v_mov_b32_dpp v126, v124 quad_perm:[2,3,0,1] row_mask:0xf bank_mask:0xf bound_ctrl:1
	v_mov_b32_dpp v127, v124 quad_perm:[3,0,1,2] row_mask:0xf bank_mask:0xf bound_ctrl:1
	v_pk_fma_f32 v[150:151], v[60:61], v[158:159], v[154:155]
	s_waitcnt lgkmcnt(14)
	v_mfma_f32_16x16x32_f16 v[132:135], v[6:9], v[124:127], v[68:71]
	v_cvt_pk_f16_f32 v128, v150, v151
	s_nop 0
	v_mfma_f32_16x16x32_f16 v[136:139], v[10:13], v[124:127], v[68:71]
	v_mov_b32_dpp v129, v128 quad_perm:[1,2,3,0] row_mask:0xf bank_mask:0xf bound_ctrl:1
	v_mov_b32_dpp v130, v128 quad_perm:[2,3,0,1] row_mask:0xf bank_mask:0xf bound_ctrl:1
	v_mfma_f32_16x16x32_f16 v[140:143], v[18:21], v[124:127], v[68:71]
	v_mov_b32_dpp v131, v128 quad_perm:[3,0,1,2] row_mask:0xf bank_mask:0xf bound_ctrl:1
	ds_write_b32 v164, v124 offset:16896
	ds_write_b32 v164, v128 offset:16900
	v_mfma_f32_16x16x32_f16 v[132:135], v[2:5], v[128:131], v[132:135]
	s_nop 1
	v_mfma_f32_16x16x32_f16 v[136:139], v[14:17], v[128:131], v[136:139]
	s_nop 1
	v_mfma_f32_16x16x32_f16 v[140:143], v[22:25], v[128:131], v[140:143]
	v_pk_fma_f32 v[154:155], v[56:57], v[150:151], v[58:59]
	v_pk_fma_f32 v[152:153], v[50:51], v[148:149], v[52:53]
	s_nop 2
	v_cndmask_b32_e64 v160, v136, v132, s[6:7]
	v_cndmask_b32_e64 v161, v137, v133, s[6:7]
	v_cndmask_b32_e64 v162, v138, v134, s[6:7]
	v_cndmask_b32_e64 v163, v139, v135, s[6:7]
	v_cndmask_b32_e64 v156, v140, v160, s[4:5]
	v_cndmask_b32_e64 v157, v141, v161, s[4:5]
	v_exp_f32_e32 v156, v156
	v_exp_f32_e32 v157, v157
	v_cndmask_b32_e64 v158, v142, v162, s[4:5]
	v_cndmask_b32_e64 v159, v143, v163, s[4:5]
	v_pk_add_f32 v[156:157], v[156:157], 1.0 op_sel_hi:[1,0]
	v_exp_f32_e32 v158, v158
	v_rcp_f32_e32 v156, v156
	v_rcp_f32_e32 v157, v157
	v_exp_f32_e32 v159, v159
	v_pk_fma_f32 v[148:149], v[54:55], v[156:157], v[152:153]
	v_pk_add_f32 v[158:159], v[158:159], 1.0 op_sel_hi:[1,0]
	v_cvt_pk_f16_f32 v124, v148, v149
	v_rcp_f32_e32 v158, v158
	v_rcp_f32_e32 v159, v159
	v_mov_b32_dpp v125, v124 quad_perm:[1,2,3,0] row_mask:0xf bank_mask:0xf bound_ctrl:1
	v_mov_b32_dpp v126, v124 quad_perm:[2,3,0,1] row_mask:0xf bank_mask:0xf bound_ctrl:1
	v_mov_b32_dpp v127, v124 quad_perm:[3,0,1,2] row_mask:0xf bank_mask:0xf bound_ctrl:1
	v_pk_fma_f32 v[150:151], v[60:61], v[158:159], v[154:155]
	s_waitcnt lgkmcnt(15)
	v_mfma_f32_16x16x32_f16 v[132:135], v[6:9], v[124:127], v[72:75]
	v_cvt_pk_f16_f32 v128, v150, v151
	s_nop 0
	v_mfma_f32_16x16x32_f16 v[136:139], v[10:13], v[124:127], v[72:75]
	v_mov_b32_dpp v129, v128 quad_perm:[1,2,3,0] row_mask:0xf bank_mask:0xf bound_ctrl:1
	v_mov_b32_dpp v130, v128 quad_perm:[2,3,0,1] row_mask:0xf bank_mask:0xf bound_ctrl:1
	v_mfma_f32_16x16x32_f16 v[140:143], v[18:21], v[124:127], v[72:75]
	v_mov_b32_dpp v131, v128 quad_perm:[3,0,1,2] row_mask:0xf bank_mask:0xf bound_ctrl:1
	ds_write_b32 v164, v124 offset:17424
	ds_write_b32 v164, v128 offset:17428
	v_mfma_f32_16x16x32_f16 v[132:135], v[2:5], v[128:131], v[132:135]
	s_nop 1
	v_mfma_f32_16x16x32_f16 v[136:139], v[14:17], v[128:131], v[136:139]
	s_nop 1
	v_mfma_f32_16x16x32_f16 v[140:143], v[22:25], v[128:131], v[140:143]
	v_pk_fma_f32 v[154:155], v[56:57], v[150:151], v[58:59]
	v_pk_fma_f32 v[152:153], v[50:51], v[148:149], v[52:53]
	s_nop 2
	v_cndmask_b32_e64 v160, v136, v132, s[6:7]
	v_cndmask_b32_e64 v161, v137, v133, s[6:7]
	v_cndmask_b32_e64 v162, v138, v134, s[6:7]
	v_cndmask_b32_e64 v163, v139, v135, s[6:7]
	v_cndmask_b32_e64 v156, v140, v160, s[4:5]
	v_cndmask_b32_e64 v157, v141, v161, s[4:5]
	v_exp_f32_e32 v156, v156
	v_exp_f32_e32 v157, v157
	v_cndmask_b32_e64 v158, v142, v162, s[4:5]
	v_cndmask_b32_e64 v159, v143, v163, s[4:5]
	v_pk_add_f32 v[156:157], v[156:157], 1.0 op_sel_hi:[1,0]
	v_exp_f32_e32 v158, v158
	v_rcp_f32_e32 v156, v156
	v_rcp_f32_e32 v157, v157
	v_exp_f32_e32 v159, v159
	v_pk_fma_f32 v[148:149], v[54:55], v[156:157], v[152:153]
	v_pk_add_f32 v[158:159], v[158:159], 1.0 op_sel_hi:[1,0]
	v_cvt_pk_f16_f32 v124, v148, v149
	v_rcp_f32_e32 v158, v158
	v_rcp_f32_e32 v159, v159
	v_mov_b32_dpp v125, v124 quad_perm:[1,2,3,0] row_mask:0xf bank_mask:0xf bound_ctrl:1
	v_mov_b32_dpp v126, v124 quad_perm:[2,3,0,1] row_mask:0xf bank_mask:0xf bound_ctrl:1
	v_mov_b32_dpp v127, v124 quad_perm:[3,0,1,2] row_mask:0xf bank_mask:0xf bound_ctrl:1
	v_pk_fma_f32 v[150:151], v[60:61], v[158:159], v[154:155]
	s_waitcnt lgkmcnt(15)
	v_mfma_f32_16x16x32_f16 v[132:135], v[6:9], v[124:127], v[76:79]
	v_cvt_pk_f16_f32 v128, v150, v151
	s_nop 0
	v_mfma_f32_16x16x32_f16 v[136:139], v[10:13], v[124:127], v[76:79]
	v_mov_b32_dpp v129, v128 quad_perm:[1,2,3,0] row_mask:0xf bank_mask:0xf bound_ctrl:1
	v_mov_b32_dpp v130, v128 quad_perm:[2,3,0,1] row_mask:0xf bank_mask:0xf bound_ctrl:1
	v_mfma_f32_16x16x32_f16 v[140:143], v[18:21], v[124:127], v[76:79]
	v_mov_b32_dpp v131, v128 quad_perm:[3,0,1,2] row_mask:0xf bank_mask:0xf bound_ctrl:1
	ds_write_b32 v164, v124 offset:17952
	ds_write_b32 v164, v128 offset:17956
	v_mfma_f32_16x16x32_f16 v[132:135], v[2:5], v[128:131], v[132:135]
	s_nop 1
	v_mfma_f32_16x16x32_f16 v[136:139], v[14:17], v[128:131], v[136:139]
	s_nop 1
	v_mfma_f32_16x16x32_f16 v[140:143], v[22:25], v[128:131], v[140:143]
	v_pk_fma_f32 v[154:155], v[56:57], v[150:151], v[58:59]
	v_pk_fma_f32 v[152:153], v[50:51], v[148:149], v[52:53]
	s_nop 2
	v_cndmask_b32_e64 v160, v136, v132, s[6:7]
	v_cndmask_b32_e64 v161, v137, v133, s[6:7]
	v_cndmask_b32_e64 v162, v138, v134, s[6:7]
	v_cndmask_b32_e64 v163, v139, v135, s[6:7]
	v_cndmask_b32_e64 v156, v140, v160, s[4:5]
	v_cndmask_b32_e64 v157, v141, v161, s[4:5]
	v_exp_f32_e32 v156, v156
	v_exp_f32_e32 v157, v157
	v_cndmask_b32_e64 v158, v142, v162, s[4:5]
	v_cndmask_b32_e64 v159, v143, v163, s[4:5]
	v_pk_add_f32 v[156:157], v[156:157], 1.0 op_sel_hi:[1,0]
	v_exp_f32_e32 v158, v158
	v_rcp_f32_e32 v156, v156
	v_rcp_f32_e32 v157, v157
	v_exp_f32_e32 v159, v159
	v_pk_fma_f32 v[148:149], v[54:55], v[156:157], v[152:153]
	v_pk_add_f32 v[158:159], v[158:159], 1.0 op_sel_hi:[1,0]
	v_cvt_pk_f16_f32 v124, v148, v149
	v_rcp_f32_e32 v158, v158
	v_rcp_f32_e32 v159, v159
	v_mov_b32_dpp v125, v124 quad_perm:[1,2,3,0] row_mask:0xf bank_mask:0xf bound_ctrl:1
	v_mov_b32_dpp v126, v124 quad_perm:[2,3,0,1] row_mask:0xf bank_mask:0xf bound_ctrl:1
	v_mov_b32_dpp v127, v124 quad_perm:[3,0,1,2] row_mask:0xf bank_mask:0xf bound_ctrl:1
	v_pk_fma_f32 v[150:151], v[60:61], v[158:159], v[154:155]
	s_waitcnt lgkmcnt(15)
	v_mfma_f32_16x16x32_f16 v[132:135], v[6:9], v[124:127], v[80:83]
	v_cvt_pk_f16_f32 v128, v150, v151
	s_nop 0
	v_mfma_f32_16x16x32_f16 v[136:139], v[10:13], v[124:127], v[80:83]
	v_mov_b32_dpp v129, v128 quad_perm:[1,2,3,0] row_mask:0xf bank_mask:0xf bound_ctrl:1
	v_mov_b32_dpp v130, v128 quad_perm:[2,3,0,1] row_mask:0xf bank_mask:0xf bound_ctrl:1
	v_mfma_f32_16x16x32_f16 v[140:143], v[18:21], v[124:127], v[80:83]
	v_mov_b32_dpp v131, v128 quad_perm:[3,0,1,2] row_mask:0xf bank_mask:0xf bound_ctrl:1
	ds_write_b32 v164, v124 offset:18480
	ds_write_b32 v164, v128 offset:18484
	v_mfma_f32_16x16x32_f16 v[132:135], v[2:5], v[128:131], v[132:135]
	s_nop 1
	v_mfma_f32_16x16x32_f16 v[136:139], v[14:17], v[128:131], v[136:139]
	s_nop 1
	v_mfma_f32_16x16x32_f16 v[140:143], v[22:25], v[128:131], v[140:143]
	v_pk_fma_f32 v[154:155], v[56:57], v[150:151], v[58:59]
	v_pk_fma_f32 v[152:153], v[50:51], v[148:149], v[52:53]
	s_nop 2
	v_cndmask_b32_e64 v160, v136, v132, s[6:7]
	v_cndmask_b32_e64 v161, v137, v133, s[6:7]
	v_cndmask_b32_e64 v162, v138, v134, s[6:7]
	v_cndmask_b32_e64 v163, v139, v135, s[6:7]
	v_cndmask_b32_e64 v156, v140, v160, s[4:5]
	v_cndmask_b32_e64 v157, v141, v161, s[4:5]
	v_exp_f32_e32 v156, v156
	v_exp_f32_e32 v157, v157
	v_cndmask_b32_e64 v158, v142, v162, s[4:5]
	v_cndmask_b32_e64 v159, v143, v163, s[4:5]
	v_pk_add_f32 v[156:157], v[156:157], 1.0 op_sel_hi:[1,0]
	v_exp_f32_e32 v158, v158
	v_rcp_f32_e32 v156, v156
	v_rcp_f32_e32 v157, v157
	v_exp_f32_e32 v159, v159
	v_pk_fma_f32 v[148:149], v[54:55], v[156:157], v[152:153]
	v_pk_add_f32 v[158:159], v[158:159], 1.0 op_sel_hi:[1,0]
	v_cvt_pk_f16_f32 v124, v148, v149
	v_rcp_f32_e32 v158, v158
	v_rcp_f32_e32 v159, v159
	v_mov_b32_dpp v125, v124 quad_perm:[1,2,3,0] row_mask:0xf bank_mask:0xf bound_ctrl:1
	v_mov_b32_dpp v126, v124 quad_perm:[2,3,0,1] row_mask:0xf bank_mask:0xf bound_ctrl:1
	v_mov_b32_dpp v127, v124 quad_perm:[3,0,1,2] row_mask:0xf bank_mask:0xf bound_ctrl:1
	v_pk_fma_f32 v[150:151], v[60:61], v[158:159], v[154:155]
	s_waitcnt lgkmcnt(15)
	v_mfma_f32_16x16x32_f16 v[132:135], v[6:9], v[124:127], v[84:87]
	v_cvt_pk_f16_f32 v128, v150, v151
	s_nop 0
	v_mfma_f32_16x16x32_f16 v[136:139], v[10:13], v[124:127], v[84:87]
	v_mov_b32_dpp v129, v128 quad_perm:[1,2,3,0] row_mask:0xf bank_mask:0xf bound_ctrl:1
	v_mov_b32_dpp v130, v128 quad_perm:[2,3,0,1] row_mask:0xf bank_mask:0xf bound_ctrl:1
	v_mfma_f32_16x16x32_f16 v[140:143], v[18:21], v[124:127], v[84:87]
	v_mov_b32_dpp v131, v128 quad_perm:[3,0,1,2] row_mask:0xf bank_mask:0xf bound_ctrl:1
	ds_write_b32 v164, v124 offset:19008
	ds_write_b32 v164, v128 offset:19012
	v_mfma_f32_16x16x32_f16 v[132:135], v[2:5], v[128:131], v[132:135]
	s_nop 1
	v_mfma_f32_16x16x32_f16 v[136:139], v[14:17], v[128:131], v[136:139]
	s_nop 1
	v_mfma_f32_16x16x32_f16 v[140:143], v[22:25], v[128:131], v[140:143]
	v_pk_fma_f32 v[154:155], v[56:57], v[150:151], v[58:59]
	v_pk_fma_f32 v[152:153], v[50:51], v[148:149], v[52:53]
	s_nop 2
	v_cndmask_b32_e64 v160, v136, v132, s[6:7]
	v_cndmask_b32_e64 v161, v137, v133, s[6:7]
	v_cndmask_b32_e64 v162, v138, v134, s[6:7]
	v_cndmask_b32_e64 v163, v139, v135, s[6:7]
	v_cndmask_b32_e64 v156, v140, v160, s[4:5]
	v_cndmask_b32_e64 v157, v141, v161, s[4:5]
	v_exp_f32_e32 v156, v156
	v_exp_f32_e32 v157, v157
	v_cndmask_b32_e64 v158, v142, v162, s[4:5]
	v_cndmask_b32_e64 v159, v143, v163, s[4:5]
	v_pk_add_f32 v[156:157], v[156:157], 1.0 op_sel_hi:[1,0]
	v_exp_f32_e32 v158, v158
	v_rcp_f32_e32 v156, v156
	v_rcp_f32_e32 v157, v157
	v_exp_f32_e32 v159, v159
	v_pk_fma_f32 v[148:149], v[54:55], v[156:157], v[152:153]
	v_pk_add_f32 v[158:159], v[158:159], 1.0 op_sel_hi:[1,0]
	v_cvt_pk_f16_f32 v124, v148, v149
	v_rcp_f32_e32 v158, v158
	v_rcp_f32_e32 v159, v159
	v_mov_b32_dpp v125, v124 quad_perm:[1,2,3,0] row_mask:0xf bank_mask:0xf bound_ctrl:1
	v_mov_b32_dpp v126, v124 quad_perm:[2,3,0,1] row_mask:0xf bank_mask:0xf bound_ctrl:1
	v_mov_b32_dpp v127, v124 quad_perm:[3,0,1,2] row_mask:0xf bank_mask:0xf bound_ctrl:1
	v_pk_fma_f32 v[150:151], v[60:61], v[158:159], v[154:155]
	s_waitcnt lgkmcnt(15)
	v_mfma_f32_16x16x32_f16 v[132:135], v[6:9], v[124:127], v[88:91]
	v_cvt_pk_f16_f32 v128, v150, v151
	s_nop 0
	v_mfma_f32_16x16x32_f16 v[136:139], v[10:13], v[124:127], v[88:91]
	v_mov_b32_dpp v129, v128 quad_perm:[1,2,3,0] row_mask:0xf bank_mask:0xf bound_ctrl:1
	v_mov_b32_dpp v130, v128 quad_perm:[2,3,0,1] row_mask:0xf bank_mask:0xf bound_ctrl:1
	v_mfma_f32_16x16x32_f16 v[140:143], v[18:21], v[124:127], v[88:91]
	v_mov_b32_dpp v131, v128 quad_perm:[3,0,1,2] row_mask:0xf bank_mask:0xf bound_ctrl:1
	ds_write_b32 v164, v124 offset:19536
	ds_write_b32 v164, v128 offset:19540
	v_mfma_f32_16x16x32_f16 v[132:135], v[2:5], v[128:131], v[132:135]
	s_nop 1
	v_mfma_f32_16x16x32_f16 v[136:139], v[14:17], v[128:131], v[136:139]
	s_nop 1
	v_mfma_f32_16x16x32_f16 v[140:143], v[22:25], v[128:131], v[140:143]
	v_pk_fma_f32 v[154:155], v[56:57], v[150:151], v[58:59]
	v_pk_fma_f32 v[152:153], v[50:51], v[148:149], v[52:53]
	s_nop 2
	v_cndmask_b32_e64 v160, v136, v132, s[6:7]
	v_cndmask_b32_e64 v161, v137, v133, s[6:7]
	v_cndmask_b32_e64 v162, v138, v134, s[6:7]
	v_cndmask_b32_e64 v163, v139, v135, s[6:7]
	v_cndmask_b32_e64 v156, v140, v160, s[4:5]
	v_cndmask_b32_e64 v157, v141, v161, s[4:5]
	v_exp_f32_e32 v156, v156
	v_exp_f32_e32 v157, v157
	v_cndmask_b32_e64 v158, v142, v162, s[4:5]
	v_cndmask_b32_e64 v159, v143, v163, s[4:5]
	v_pk_add_f32 v[156:157], v[156:157], 1.0 op_sel_hi:[1,0]
	v_exp_f32_e32 v158, v158
	v_rcp_f32_e32 v156, v156
	v_rcp_f32_e32 v157, v157
	v_exp_f32_e32 v159, v159
	v_pk_fma_f32 v[148:149], v[54:55], v[156:157], v[152:153]
	v_pk_add_f32 v[158:159], v[158:159], 1.0 op_sel_hi:[1,0]
	v_cvt_pk_f16_f32 v124, v148, v149
	v_rcp_f32_e32 v158, v158
	v_rcp_f32_e32 v159, v159
	v_mov_b32_dpp v125, v124 quad_perm:[1,2,3,0] row_mask:0xf bank_mask:0xf bound_ctrl:1
	v_mov_b32_dpp v126, v124 quad_perm:[2,3,0,1] row_mask:0xf bank_mask:0xf bound_ctrl:1
	v_mov_b32_dpp v127, v124 quad_perm:[3,0,1,2] row_mask:0xf bank_mask:0xf bound_ctrl:1
	v_pk_fma_f32 v[150:151], v[60:61], v[158:159], v[154:155]
	s_waitcnt lgkmcnt(15)
	v_mfma_f32_16x16x32_f16 v[132:135], v[6:9], v[124:127], v[92:95]
	v_cvt_pk_f16_f32 v128, v150, v151
	s_nop 0
	v_mfma_f32_16x16x32_f16 v[136:139], v[10:13], v[124:127], v[92:95]
	v_mov_b32_dpp v129, v128 quad_perm:[1,2,3,0] row_mask:0xf bank_mask:0xf bound_ctrl:1
	v_mov_b32_dpp v130, v128 quad_perm:[2,3,0,1] row_mask:0xf bank_mask:0xf bound_ctrl:1
	v_mfma_f32_16x16x32_f16 v[140:143], v[18:21], v[124:127], v[92:95]
	v_mov_b32_dpp v131, v128 quad_perm:[3,0,1,2] row_mask:0xf bank_mask:0xf bound_ctrl:1
	ds_write_b32 v164, v124 offset:20064
	ds_write_b32 v164, v128 offset:20068
	v_mfma_f32_16x16x32_f16 v[132:135], v[2:5], v[128:131], v[132:135]
	s_nop 1
	v_mfma_f32_16x16x32_f16 v[136:139], v[14:17], v[128:131], v[136:139]
	s_nop 1
	v_mfma_f32_16x16x32_f16 v[140:143], v[22:25], v[128:131], v[140:143]
	v_pk_fma_f32 v[154:155], v[56:57], v[150:151], v[58:59]
	v_pk_fma_f32 v[152:153], v[50:51], v[148:149], v[52:53]
	s_nop 2
	v_cndmask_b32_e64 v160, v136, v132, s[6:7]
	v_cndmask_b32_e64 v161, v137, v133, s[6:7]
	v_cndmask_b32_e64 v162, v138, v134, s[6:7]
	v_cndmask_b32_e64 v163, v139, v135, s[6:7]
	v_cndmask_b32_e64 v156, v140, v160, s[4:5]
	v_cndmask_b32_e64 v157, v141, v161, s[4:5]
	v_exp_f32_e32 v156, v156
	v_exp_f32_e32 v157, v157
	v_cndmask_b32_e64 v158, v142, v162, s[4:5]
	v_cndmask_b32_e64 v159, v143, v163, s[4:5]
	v_pk_add_f32 v[156:157], v[156:157], 1.0 op_sel_hi:[1,0]
	v_exp_f32_e32 v158, v158
	v_rcp_f32_e32 v156, v156
	v_rcp_f32_e32 v157, v157
	v_exp_f32_e32 v159, v159
	v_pk_fma_f32 v[148:149], v[54:55], v[156:157], v[152:153]
	v_pk_add_f32 v[158:159], v[158:159], 1.0 op_sel_hi:[1,0]
	v_cvt_pk_f16_f32 v124, v148, v149
	v_rcp_f32_e32 v158, v158
	v_rcp_f32_e32 v159, v159
	v_mov_b32_dpp v125, v124 quad_perm:[1,2,3,0] row_mask:0xf bank_mask:0xf bound_ctrl:1
	v_mov_b32_dpp v126, v124 quad_perm:[2,3,0,1] row_mask:0xf bank_mask:0xf bound_ctrl:1
	v_mov_b32_dpp v127, v124 quad_perm:[3,0,1,2] row_mask:0xf bank_mask:0xf bound_ctrl:1
	v_pk_fma_f32 v[150:151], v[60:61], v[158:159], v[154:155]
	s_waitcnt lgkmcnt(15)
	v_mfma_f32_16x16x32_f16 v[132:135], v[6:9], v[124:127], v[96:99]
	v_cvt_pk_f16_f32 v128, v150, v151
	s_nop 0
	v_mfma_f32_16x16x32_f16 v[136:139], v[10:13], v[124:127], v[96:99]
	v_mov_b32_dpp v129, v128 quad_perm:[1,2,3,0] row_mask:0xf bank_mask:0xf bound_ctrl:1
	v_mov_b32_dpp v130, v128 quad_perm:[2,3,0,1] row_mask:0xf bank_mask:0xf bound_ctrl:1
	v_mfma_f32_16x16x32_f16 v[140:143], v[18:21], v[124:127], v[96:99]
	v_mov_b32_dpp v131, v128 quad_perm:[3,0,1,2] row_mask:0xf bank_mask:0xf bound_ctrl:1
	ds_write_b32 v164, v124 offset:20592
	ds_write_b32 v164, v128 offset:20596
	v_mfma_f32_16x16x32_f16 v[132:135], v[2:5], v[128:131], v[132:135]
	s_nop 1
	v_mfma_f32_16x16x32_f16 v[136:139], v[14:17], v[128:131], v[136:139]
	s_nop 1
	v_mfma_f32_16x16x32_f16 v[140:143], v[22:25], v[128:131], v[140:143]
	v_pk_fma_f32 v[154:155], v[56:57], v[150:151], v[58:59]
	v_pk_fma_f32 v[152:153], v[50:51], v[148:149], v[52:53]
	s_nop 2
	v_cndmask_b32_e64 v160, v136, v132, s[6:7]
	v_cndmask_b32_e64 v161, v137, v133, s[6:7]
	v_cndmask_b32_e64 v162, v138, v134, s[6:7]
	v_cndmask_b32_e64 v163, v139, v135, s[6:7]
	v_cndmask_b32_e64 v156, v140, v160, s[4:5]
	v_cndmask_b32_e64 v157, v141, v161, s[4:5]
	v_exp_f32_e32 v156, v156
	v_exp_f32_e32 v157, v157
	v_cndmask_b32_e64 v158, v142, v162, s[4:5]
	v_cndmask_b32_e64 v159, v143, v163, s[4:5]
	v_pk_add_f32 v[156:157], v[156:157], 1.0 op_sel_hi:[1,0]
	v_exp_f32_e32 v158, v158
	v_rcp_f32_e32 v156, v156
	v_rcp_f32_e32 v157, v157
	v_exp_f32_e32 v159, v159
	v_pk_fma_f32 v[148:149], v[54:55], v[156:157], v[152:153]
	v_pk_add_f32 v[158:159], v[158:159], 1.0 op_sel_hi:[1,0]
	v_cvt_pk_f16_f32 v124, v148, v149
	v_rcp_f32_e32 v158, v158
	v_rcp_f32_e32 v159, v159
	v_mov_b32_dpp v125, v124 quad_perm:[1,2,3,0] row_mask:0xf bank_mask:0xf bound_ctrl:1
	v_mov_b32_dpp v126, v124 quad_perm:[2,3,0,1] row_mask:0xf bank_mask:0xf bound_ctrl:1
	v_mov_b32_dpp v127, v124 quad_perm:[3,0,1,2] row_mask:0xf bank_mask:0xf bound_ctrl:1
	v_pk_fma_f32 v[150:151], v[60:61], v[158:159], v[154:155]
	s_waitcnt lgkmcnt(15)
	v_mfma_f32_16x16x32_f16 v[132:135], v[6:9], v[124:127], v[100:103]
	v_cvt_pk_f16_f32 v128, v150, v151
	s_nop 0
	v_mfma_f32_16x16x32_f16 v[136:139], v[10:13], v[124:127], v[100:103]
	v_mov_b32_dpp v129, v128 quad_perm:[1,2,3,0] row_mask:0xf bank_mask:0xf bound_ctrl:1
	v_mov_b32_dpp v130, v128 quad_perm:[2,3,0,1] row_mask:0xf bank_mask:0xf bound_ctrl:1
	v_mfma_f32_16x16x32_f16 v[140:143], v[18:21], v[124:127], v[100:103]
	v_mov_b32_dpp v131, v128 quad_perm:[3,0,1,2] row_mask:0xf bank_mask:0xf bound_ctrl:1
	ds_write_b32 v164, v124 offset:21120
	ds_write_b32 v164, v128 offset:21124
	v_mfma_f32_16x16x32_f16 v[132:135], v[2:5], v[128:131], v[132:135]
	s_nop 1
	v_mfma_f32_16x16x32_f16 v[136:139], v[14:17], v[128:131], v[136:139]
	s_nop 1
	v_mfma_f32_16x16x32_f16 v[140:143], v[22:25], v[128:131], v[140:143]
	v_pk_fma_f32 v[154:155], v[56:57], v[150:151], v[58:59]
	v_pk_fma_f32 v[152:153], v[50:51], v[148:149], v[52:53]
	s_nop 2
	v_cndmask_b32_e64 v160, v136, v132, s[6:7]
	v_cndmask_b32_e64 v161, v137, v133, s[6:7]
	v_cndmask_b32_e64 v162, v138, v134, s[6:7]
	v_cndmask_b32_e64 v163, v139, v135, s[6:7]
	v_cndmask_b32_e64 v156, v140, v160, s[4:5]
	v_cndmask_b32_e64 v157, v141, v161, s[4:5]
	v_exp_f32_e32 v156, v156
	v_exp_f32_e32 v157, v157
	v_cndmask_b32_e64 v158, v142, v162, s[4:5]
	v_cndmask_b32_e64 v159, v143, v163, s[4:5]
	v_pk_add_f32 v[156:157], v[156:157], 1.0 op_sel_hi:[1,0]
	v_exp_f32_e32 v158, v158
	v_rcp_f32_e32 v156, v156
	v_rcp_f32_e32 v157, v157
	v_exp_f32_e32 v159, v159
	v_pk_fma_f32 v[148:149], v[54:55], v[156:157], v[152:153]
	v_pk_add_f32 v[158:159], v[158:159], 1.0 op_sel_hi:[1,0]
	v_cvt_pk_f16_f32 v124, v148, v149
	v_rcp_f32_e32 v158, v158
	v_rcp_f32_e32 v159, v159
	v_mov_b32_dpp v125, v124 quad_perm:[1,2,3,0] row_mask:0xf bank_mask:0xf bound_ctrl:1
	v_mov_b32_dpp v126, v124 quad_perm:[2,3,0,1] row_mask:0xf bank_mask:0xf bound_ctrl:1
	v_mov_b32_dpp v127, v124 quad_perm:[3,0,1,2] row_mask:0xf bank_mask:0xf bound_ctrl:1
	v_pk_fma_f32 v[150:151], v[60:61], v[158:159], v[154:155]
	s_waitcnt lgkmcnt(15)
	v_mfma_f32_16x16x32_f16 v[132:135], v[6:9], v[124:127], v[104:107]
	v_cvt_pk_f16_f32 v128, v150, v151
	s_nop 0
	v_mfma_f32_16x16x32_f16 v[136:139], v[10:13], v[124:127], v[104:107]
	v_mov_b32_dpp v129, v128 quad_perm:[1,2,3,0] row_mask:0xf bank_mask:0xf bound_ctrl:1
	v_mov_b32_dpp v130, v128 quad_perm:[2,3,0,1] row_mask:0xf bank_mask:0xf bound_ctrl:1
	v_mfma_f32_16x16x32_f16 v[140:143], v[18:21], v[124:127], v[104:107]
	v_mov_b32_dpp v131, v128 quad_perm:[3,0,1,2] row_mask:0xf bank_mask:0xf bound_ctrl:1
	ds_write_b32 v164, v124 offset:21648
	ds_write_b32 v164, v128 offset:21652
	v_mfma_f32_16x16x32_f16 v[132:135], v[2:5], v[128:131], v[132:135]
	s_nop 1
	v_mfma_f32_16x16x32_f16 v[136:139], v[14:17], v[128:131], v[136:139]
	s_nop 1
	v_mfma_f32_16x16x32_f16 v[140:143], v[22:25], v[128:131], v[140:143]
	v_pk_fma_f32 v[154:155], v[56:57], v[150:151], v[58:59]
	v_pk_fma_f32 v[152:153], v[50:51], v[148:149], v[52:53]
	s_nop 2
	v_cndmask_b32_e64 v160, v136, v132, s[6:7]
	v_cndmask_b32_e64 v161, v137, v133, s[6:7]
	v_cndmask_b32_e64 v162, v138, v134, s[6:7]
	v_cndmask_b32_e64 v163, v139, v135, s[6:7]
	v_cndmask_b32_e64 v156, v140, v160, s[4:5]
	v_cndmask_b32_e64 v157, v141, v161, s[4:5]
	v_exp_f32_e32 v156, v156
	v_exp_f32_e32 v157, v157
	v_cndmask_b32_e64 v158, v142, v162, s[4:5]
	v_cndmask_b32_e64 v159, v143, v163, s[4:5]
	v_pk_add_f32 v[156:157], v[156:157], 1.0 op_sel_hi:[1,0]
	v_exp_f32_e32 v158, v158
	v_rcp_f32_e32 v156, v156
	v_rcp_f32_e32 v157, v157
	v_exp_f32_e32 v159, v159
	v_pk_fma_f32 v[148:149], v[54:55], v[156:157], v[152:153]
	v_pk_add_f32 v[158:159], v[158:159], 1.0 op_sel_hi:[1,0]
	v_cvt_pk_f16_f32 v124, v148, v149
	v_rcp_f32_e32 v158, v158
	v_rcp_f32_e32 v159, v159
	v_mov_b32_dpp v125, v124 quad_perm:[1,2,3,0] row_mask:0xf bank_mask:0xf bound_ctrl:1
	v_mov_b32_dpp v126, v124 quad_perm:[2,3,0,1] row_mask:0xf bank_mask:0xf bound_ctrl:1
	v_mov_b32_dpp v127, v124 quad_perm:[3,0,1,2] row_mask:0xf bank_mask:0xf bound_ctrl:1
	v_pk_fma_f32 v[150:151], v[60:61], v[158:159], v[154:155]
	s_waitcnt lgkmcnt(15)
	v_mfma_f32_16x16x32_f16 v[132:135], v[6:9], v[124:127], v[108:111]
	v_cvt_pk_f16_f32 v128, v150, v151
	s_nop 0
	v_mfma_f32_16x16x32_f16 v[136:139], v[10:13], v[124:127], v[108:111]
	v_mov_b32_dpp v129, v128 quad_perm:[1,2,3,0] row_mask:0xf bank_mask:0xf bound_ctrl:1
	v_mov_b32_dpp v130, v128 quad_perm:[2,3,0,1] row_mask:0xf bank_mask:0xf bound_ctrl:1
	v_mfma_f32_16x16x32_f16 v[140:143], v[18:21], v[124:127], v[108:111]
	v_mov_b32_dpp v131, v128 quad_perm:[3,0,1,2] row_mask:0xf bank_mask:0xf bound_ctrl:1
	ds_write_b32 v164, v124 offset:22176
	ds_write_b32 v164, v128 offset:22180
	v_mfma_f32_16x16x32_f16 v[132:135], v[2:5], v[128:131], v[132:135]
	s_nop 1
	v_mfma_f32_16x16x32_f16 v[136:139], v[14:17], v[128:131], v[136:139]
	s_nop 1
	v_mfma_f32_16x16x32_f16 v[140:143], v[22:25], v[128:131], v[140:143]
	v_pk_fma_f32 v[154:155], v[56:57], v[150:151], v[58:59]
	v_pk_fma_f32 v[152:153], v[50:51], v[148:149], v[52:53]
	s_nop 2
	v_cndmask_b32_e64 v160, v136, v132, s[6:7]
	v_cndmask_b32_e64 v161, v137, v133, s[6:7]
	v_cndmask_b32_e64 v162, v138, v134, s[6:7]
	v_cndmask_b32_e64 v163, v139, v135, s[6:7]
	v_cndmask_b32_e64 v156, v140, v160, s[4:5]
	v_cndmask_b32_e64 v157, v141, v161, s[4:5]
	v_exp_f32_e32 v156, v156
	v_exp_f32_e32 v157, v157
	v_cndmask_b32_e64 v158, v142, v162, s[4:5]
	v_cndmask_b32_e64 v159, v143, v163, s[4:5]
	v_pk_add_f32 v[156:157], v[156:157], 1.0 op_sel_hi:[1,0]
	v_exp_f32_e32 v158, v158
	v_rcp_f32_e32 v156, v156
	v_rcp_f32_e32 v157, v157
	v_exp_f32_e32 v159, v159
	v_pk_fma_f32 v[148:149], v[54:55], v[156:157], v[152:153]
	v_pk_add_f32 v[158:159], v[158:159], 1.0 op_sel_hi:[1,0]
	v_cvt_pk_f16_f32 v124, v148, v149
	v_rcp_f32_e32 v158, v158
	v_rcp_f32_e32 v159, v159
	v_mov_b32_dpp v125, v124 quad_perm:[1,2,3,0] row_mask:0xf bank_mask:0xf bound_ctrl:1
	v_mov_b32_dpp v126, v124 quad_perm:[2,3,0,1] row_mask:0xf bank_mask:0xf bound_ctrl:1
	v_mov_b32_dpp v127, v124 quad_perm:[3,0,1,2] row_mask:0xf bank_mask:0xf bound_ctrl:1
	v_pk_fma_f32 v[150:151], v[60:61], v[158:159], v[154:155]
	s_waitcnt lgkmcnt(15)
	v_mfma_f32_16x16x32_f16 v[132:135], v[6:9], v[124:127], v[112:115]
	v_cvt_pk_f16_f32 v128, v150, v151
	s_nop 0
	v_mfma_f32_16x16x32_f16 v[136:139], v[10:13], v[124:127], v[112:115]
	v_mov_b32_dpp v129, v128 quad_perm:[1,2,3,0] row_mask:0xf bank_mask:0xf bound_ctrl:1
	v_mov_b32_dpp v130, v128 quad_perm:[2,3,0,1] row_mask:0xf bank_mask:0xf bound_ctrl:1
	v_mfma_f32_16x16x32_f16 v[140:143], v[18:21], v[124:127], v[112:115]
	v_mov_b32_dpp v131, v128 quad_perm:[3,0,1,2] row_mask:0xf bank_mask:0xf bound_ctrl:1
	ds_write_b32 v164, v124 offset:22704
	ds_write_b32 v164, v128 offset:22708
	v_mfma_f32_16x16x32_f16 v[132:135], v[2:5], v[128:131], v[132:135]
	s_nop 1
	v_mfma_f32_16x16x32_f16 v[136:139], v[14:17], v[128:131], v[136:139]
	s_nop 1
	v_mfma_f32_16x16x32_f16 v[140:143], v[22:25], v[128:131], v[140:143]
	v_pk_fma_f32 v[154:155], v[56:57], v[150:151], v[58:59]
	v_pk_fma_f32 v[152:153], v[50:51], v[148:149], v[52:53]
	s_nop 2
	v_cndmask_b32_e64 v160, v136, v132, s[6:7]
	v_cndmask_b32_e64 v161, v137, v133, s[6:7]
	v_cndmask_b32_e64 v162, v138, v134, s[6:7]
	v_cndmask_b32_e64 v163, v139, v135, s[6:7]
	v_cndmask_b32_e64 v156, v140, v160, s[4:5]
	v_cndmask_b32_e64 v157, v141, v161, s[4:5]
	v_exp_f32_e32 v156, v156
	v_exp_f32_e32 v157, v157
	v_cndmask_b32_e64 v158, v142, v162, s[4:5]
	v_cndmask_b32_e64 v159, v143, v163, s[4:5]
	v_pk_add_f32 v[156:157], v[156:157], 1.0 op_sel_hi:[1,0]
	v_exp_f32_e32 v158, v158
	v_rcp_f32_e32 v156, v156
	v_rcp_f32_e32 v157, v157
	v_exp_f32_e32 v159, v159
	v_pk_fma_f32 v[148:149], v[54:55], v[156:157], v[152:153]
	v_pk_add_f32 v[158:159], v[158:159], 1.0 op_sel_hi:[1,0]
	v_cvt_pk_f16_f32 v124, v148, v149
	v_rcp_f32_e32 v158, v158
	v_rcp_f32_e32 v159, v159
	v_mov_b32_dpp v125, v124 quad_perm:[1,2,3,0] row_mask:0xf bank_mask:0xf bound_ctrl:1
	v_mov_b32_dpp v126, v124 quad_perm:[2,3,0,1] row_mask:0xf bank_mask:0xf bound_ctrl:1
	v_mov_b32_dpp v127, v124 quad_perm:[3,0,1,2] row_mask:0xf bank_mask:0xf bound_ctrl:1
	v_pk_fma_f32 v[150:151], v[60:61], v[158:159], v[154:155]
	s_waitcnt lgkmcnt(15)
	v_mfma_f32_16x16x32_f16 v[132:135], v[6:9], v[124:127], v[116:119]
	v_cvt_pk_f16_f32 v128, v150, v151
	s_nop 0
	v_mfma_f32_16x16x32_f16 v[136:139], v[10:13], v[124:127], v[116:119]
	v_mov_b32_dpp v129, v128 quad_perm:[1,2,3,0] row_mask:0xf bank_mask:0xf bound_ctrl:1
	v_mov_b32_dpp v130, v128 quad_perm:[2,3,0,1] row_mask:0xf bank_mask:0xf bound_ctrl:1
	v_mfma_f32_16x16x32_f16 v[140:143], v[18:21], v[124:127], v[116:119]
	v_mov_b32_dpp v131, v128 quad_perm:[3,0,1,2] row_mask:0xf bank_mask:0xf bound_ctrl:1
	ds_write_b32 v164, v124 offset:23232
	ds_write_b32 v164, v128 offset:23236
	v_mfma_f32_16x16x32_f16 v[132:135], v[2:5], v[128:131], v[132:135]
	s_nop 1
	v_mfma_f32_16x16x32_f16 v[136:139], v[14:17], v[128:131], v[136:139]
	s_nop 1
	v_mfma_f32_16x16x32_f16 v[140:143], v[22:25], v[128:131], v[140:143]
	v_pk_fma_f32 v[154:155], v[56:57], v[150:151], v[58:59]
	v_pk_fma_f32 v[152:153], v[50:51], v[148:149], v[52:53]
	s_nop 2
	v_cndmask_b32_e64 v160, v136, v132, s[6:7]
	v_cndmask_b32_e64 v161, v137, v133, s[6:7]
	v_cndmask_b32_e64 v162, v138, v134, s[6:7]
	v_cndmask_b32_e64 v163, v139, v135, s[6:7]
	v_cndmask_b32_e64 v156, v140, v160, s[4:5]
	v_cndmask_b32_e64 v157, v141, v161, s[4:5]
	v_exp_f32_e32 v156, v156
	v_exp_f32_e32 v157, v157
	v_cndmask_b32_e64 v158, v142, v162, s[4:5]
	v_cndmask_b32_e64 v159, v143, v163, s[4:5]
	v_pk_add_f32 v[156:157], v[156:157], 1.0 op_sel_hi:[1,0]
	v_exp_f32_e32 v158, v158
	v_rcp_f32_e32 v156, v156
	v_rcp_f32_e32 v157, v157
	v_exp_f32_e32 v159, v159
	v_pk_fma_f32 v[148:149], v[54:55], v[156:157], v[152:153]
	v_pk_add_f32 v[158:159], v[158:159], 1.0 op_sel_hi:[1,0]
	v_cvt_pk_f16_f32 v124, v148, v149
	v_rcp_f32_e32 v158, v158
	v_rcp_f32_e32 v159, v159
	v_mov_b32_dpp v125, v124 quad_perm:[1,2,3,0] row_mask:0xf bank_mask:0xf bound_ctrl:1
	v_mov_b32_dpp v126, v124 quad_perm:[2,3,0,1] row_mask:0xf bank_mask:0xf bound_ctrl:1
	v_mov_b32_dpp v127, v124 quad_perm:[3,0,1,2] row_mask:0xf bank_mask:0xf bound_ctrl:1
	v_pk_fma_f32 v[150:151], v[60:61], v[158:159], v[154:155]
	s_waitcnt lgkmcnt(15)
	v_mfma_f32_16x16x32_f16 v[132:135], v[6:9], v[124:127], v[120:123]
	v_cvt_pk_f16_f32 v128, v150, v151
	s_nop 0
	v_mfma_f32_16x16x32_f16 v[136:139], v[10:13], v[124:127], v[120:123]
	v_mov_b32_dpp v129, v128 quad_perm:[1,2,3,0] row_mask:0xf bank_mask:0xf bound_ctrl:1
	v_mov_b32_dpp v130, v128 quad_perm:[2,3,0,1] row_mask:0xf bank_mask:0xf bound_ctrl:1
	v_mfma_f32_16x16x32_f16 v[140:143], v[18:21], v[124:127], v[120:123]
	v_mov_b32_dpp v131, v128 quad_perm:[3,0,1,2] row_mask:0xf bank_mask:0xf bound_ctrl:1
	ds_write_b32 v164, v124 offset:23760
	ds_write_b32 v164, v128 offset:23764
	v_mfma_f32_16x16x32_f16 v[132:135], v[2:5], v[128:131], v[132:135]
	s_nop 1
	v_mfma_f32_16x16x32_f16 v[136:139], v[14:17], v[128:131], v[136:139]
	s_nop 1
	v_mfma_f32_16x16x32_f16 v[140:143], v[22:25], v[128:131], v[140:143]
	v_pk_fma_f32 v[154:155], v[56:57], v[150:151], v[58:59]
	v_pk_fma_f32 v[152:153], v[50:51], v[148:149], v[52:53]
	s_nop 2
	v_cndmask_b32_e64 v160, v136, v132, s[6:7]
	v_cndmask_b32_e64 v161, v137, v133, s[6:7]
	v_cndmask_b32_e64 v162, v138, v134, s[6:7]
	v_cndmask_b32_e64 v163, v139, v135, s[6:7]
	v_cndmask_b32_e64 v156, v140, v160, s[4:5]
	v_cndmask_b32_e64 v157, v141, v161, s[4:5]
	v_exp_f32_e32 v156, v156
	v_exp_f32_e32 v157, v157
	v_cndmask_b32_e64 v158, v142, v162, s[4:5]
	v_cndmask_b32_e64 v159, v143, v163, s[4:5]
	v_pk_add_f32 v[156:157], v[156:157], 1.0 op_sel_hi:[1,0]
	v_exp_f32_e32 v158, v158
	v_rcp_f32_e32 v156, v156
	v_rcp_f32_e32 v157, v157
	v_exp_f32_e32 v159, v159
	v_pk_fma_f32 v[148:149], v[54:55], v[156:157], v[152:153]
	v_pk_add_f32 v[158:159], v[158:159], 1.0 op_sel_hi:[1,0]
	v_cvt_pk_f16_f32 v124, v148, v149
	v_rcp_f32_e32 v158, v158
	v_rcp_f32_e32 v159, v159
	v_mov_b32_dpp v125, v124 quad_perm:[1,2,3,0] row_mask:0xf bank_mask:0xf bound_ctrl:1
	v_mov_b32_dpp v126, v124 quad_perm:[2,3,0,1] row_mask:0xf bank_mask:0xf bound_ctrl:1
	v_mov_b32_dpp v127, v124 quad_perm:[3,0,1,2] row_mask:0xf bank_mask:0xf bound_ctrl:1
	v_pk_fma_f32 v[150:151], v[60:61], v[158:159], v[154:155]
	s_waitcnt lgkmcnt(15)
	v_mfma_f32_16x16x32_f16 v[132:135], v[6:9], v[124:127], v[44:47]
	v_cvt_pk_f16_f32 v128, v150, v151
	s_nop 0
	v_mfma_f32_16x16x32_f16 v[136:139], v[10:13], v[124:127], v[44:47]
	v_mov_b32_dpp v129, v128 quad_perm:[1,2,3,0] row_mask:0xf bank_mask:0xf bound_ctrl:1
	v_mov_b32_dpp v130, v128 quad_perm:[2,3,0,1] row_mask:0xf bank_mask:0xf bound_ctrl:1
	v_mfma_f32_16x16x32_f16 v[140:143], v[18:21], v[124:127], v[44:47]
	v_mov_b32_dpp v131, v128 quad_perm:[3,0,1,2] row_mask:0xf bank_mask:0xf bound_ctrl:1
	ds_write_b32 v164, v124 offset:24288
	ds_write_b32 v164, v128 offset:24292
	v_mfma_f32_16x16x32_f16 v[132:135], v[2:5], v[128:131], v[132:135]
	s_nop 1
	v_mfma_f32_16x16x32_f16 v[136:139], v[14:17], v[128:131], v[136:139]
	s_nop 1
	v_mfma_f32_16x16x32_f16 v[140:143], v[22:25], v[128:131], v[140:143]
	v_pk_fma_f32 v[154:155], v[56:57], v[150:151], v[58:59]
	v_pk_fma_f32 v[152:153], v[50:51], v[148:149], v[52:53]
	s_nop 2
	v_cndmask_b32_e64 v160, v136, v132, s[6:7]
	v_cndmask_b32_e64 v161, v137, v133, s[6:7]
	v_cndmask_b32_e64 v162, v138, v134, s[6:7]
	v_cndmask_b32_e64 v163, v139, v135, s[6:7]
	v_cndmask_b32_e64 v156, v140, v160, s[4:5]
	v_cndmask_b32_e64 v157, v141, v161, s[4:5]
	v_exp_f32_e32 v156, v156
	v_exp_f32_e32 v157, v157
	v_cndmask_b32_e64 v158, v142, v162, s[4:5]
	v_cndmask_b32_e64 v159, v143, v163, s[4:5]
	v_pk_add_f32 v[156:157], v[156:157], 1.0 op_sel_hi:[1,0]
	v_exp_f32_e32 v158, v158
	v_rcp_f32_e32 v156, v156
	v_rcp_f32_e32 v157, v157
	v_exp_f32_e32 v159, v159
	v_pk_fma_f32 v[148:149], v[54:55], v[156:157], v[152:153]
	v_pk_add_f32 v[158:159], v[158:159], 1.0 op_sel_hi:[1,0]
	v_cvt_pk_f16_f32 v124, v148, v149
	v_rcp_f32_e32 v158, v158
	v_rcp_f32_e32 v159, v159
	v_mov_b32_dpp v125, v124 quad_perm:[1,2,3,0] row_mask:0xf bank_mask:0xf bound_ctrl:1
	v_mov_b32_dpp v126, v124 quad_perm:[2,3,0,1] row_mask:0xf bank_mask:0xf bound_ctrl:1
	v_mov_b32_dpp v127, v124 quad_perm:[3,0,1,2] row_mask:0xf bank_mask:0xf bound_ctrl:1
	v_pk_fma_f32 v[150:151], v[60:61], v[158:159], v[154:155]
	s_nop 0
	v_cvt_pk_f16_f32 v128, v150, v151
	ds_write_b32 v164, v124 offset:24816
	s_nop 0
	v_mov_b32_dpp v129, v128 quad_perm:[1,2,3,0] row_mask:0xf bank_mask:0xf bound_ctrl:1
	v_mov_b32_dpp v130, v128 quad_perm:[2,3,0,1] row_mask:0xf bank_mask:0xf bound_ctrl:1
	v_mov_b32_dpp v131, v128 quad_perm:[3,0,1,2] row_mask:0xf bank_mask:0xf bound_ctrl:1
	ds_write_b32 v164, v128 offset:24820
	s_branch .LBB3_48

.LBB3_169:
	s_cmp_lt_u32 s12, 64
	s_cbranch_scc1 .Lmy_l1_main
	s_cmp_lg_u32 s12, 64
	s_cbranch_scc1 .LBB3_168
	v_mov_b32_e32 v164, v122
	s_waitcnt vmcnt(15)
	v_mfma_f32_16x16x32_f16 v[132:135], v[2:5], v[124:127], v[98:101]
	v_mfma_f32_16x16x32_f16 v[136:139], v[10:13], v[124:127], v[98:101]
	v_mfma_f32_16x16x32_f16 v[140:143], v[18:21], v[124:127], v[98:101]
	v_mfma_f32_16x16x32_f16 v[144:147], v[26:29], v[124:127], v[98:101]
	v_mfma_f32_16x16x32_f16 v[132:135], v[6:9], v[128:131], v[132:135]
	s_nop 1
	v_mfma_f32_16x16x32_f16 v[136:139], v[14:17], v[128:131], v[136:139]
	s_nop 1
	v_mfma_f32_16x16x32_f16 v[140:143], v[22:25], v[128:131], v[140:143]
	s_nop 1
	v_mfma_f32_16x16x32_f16 v[144:147], v[30:33], v[128:131], v[144:147]
	v_pk_fma_f32 v[154:155], v[106:107], v[150:151], v[108:109]
	v_pk_fma_f32 v[152:153], v[102:103], v[148:149], v[104:105]
	v_cndmask_b32_e64 v160, v136, v132, s[0:1]
	v_cndmask_b32_e64 v161, v137, v133, s[0:1]
	v_cndmask_b32_e64 v162, v138, v134, s[0:1]
	v_cndmask_b32_e64 v160, v140, v160, s[2:3]
	v_cndmask_b32_e64 v161, v141, v161, s[2:3]
	v_cndmask_b32_e64 v163, v139, v135, s[0:1]
	v_cndmask_b32_e64 v156, v160, v144, s[4:5]
	v_cndmask_b32_e64 v157, v161, v145, s[4:5]
	v_exp_f32_e32 v156, v156
	v_exp_f32_e32 v157, v157
	v_cndmask_b32_e64 v162, v142, v162, s[2:3]
	v_cndmask_b32_e64 v163, v143, v163, s[2:3]
	v_cndmask_b32_e64 v158, v162, v146, s[4:5]
	v_cndmask_b32_e64 v159, v163, v147, s[4:5]
	v_pk_add_f32 v[156:157], v[156:157], 1.0 op_sel_hi:[1,0]
	v_exp_f32_e32 v158, v158
	v_rcp_f32_e32 v156, v156
	v_rcp_f32_e32 v157, v157
	v_exp_f32_e32 v159, v159
	v_pk_fma_f32 v[148:149], v[110:111], v[156:157], v[152:153]
	v_pk_add_f32 v[158:159], v[158:159], 1.0 op_sel_hi:[1,0]
	v_cvt_pk_f16_f32 v124, v148, v149
	v_rcp_f32_e32 v158, v158
	v_rcp_f32_e32 v159, v159
	v_mov_b32_dpp v125, v124 quad_perm:[1,2,3,0] row_mask:0xf bank_mask:0xf bound_ctrl:1
	v_mov_b32_dpp v126, v124 quad_perm:[2,3,0,1] row_mask:0xf bank_mask:0xf bound_ctrl:1
	v_mov_b32_dpp v127, v124 quad_perm:[3,0,1,2] row_mask:0xf bank_mask:0xf bound_ctrl:1
	v_pk_fma_f32 v[150:151], v[112:113], v[158:159], v[154:155]
	s_nop 0
	v_cvt_pk_f16_f32 v128, v150, v151
	ds_write_b32 v164, v124 offset:0
	s_nop 0
	v_mov_b32_dpp v129, v128 quad_perm:[1,2,3,0] row_mask:0xf bank_mask:0xf bound_ctrl:1
	v_mov_b32_dpp v130, v128 quad_perm:[2,3,0,1] row_mask:0xf bank_mask:0xf bound_ctrl:1
	v_mov_b32_dpp v131, v128 quad_perm:[3,0,1,2] row_mask:0xf bank_mask:0xf bound_ctrl:1
	ds_write_b32 v164, v128 offset:4
	s_branch .LBB3_168
.Lmy_l1_main:
	s_bitcmp1_b32 s12, 0
	s_cselect_b32 s10, 0x2100, 0
	s_nop 0
	v_add_u32_e32 v164, s10, v122
	s_waitcnt vmcnt(15)
	v_mfma_f32_16x16x32_f16 v[132:135], v[2:5], v[124:127], v[98:101]
	v_mfma_f32_16x16x32_f16 v[136:139], v[10:13], v[124:127], v[98:101]
	v_mfma_f32_16x16x32_f16 v[140:143], v[18:21], v[124:127], v[98:101]
	v_mfma_f32_16x16x32_f16 v[144:147], v[26:29], v[124:127], v[98:101]
	global_load_dwordx4 v[98:101], v[0:1], off offset:-2048
	v_mfma_f32_16x16x32_f16 v[132:135], v[6:9], v[128:131], v[132:135]
	s_nop 1
	v_mfma_f32_16x16x32_f16 v[136:139], v[14:17], v[128:131], v[136:139]
	s_nop 1
	v_mfma_f32_16x16x32_f16 v[140:143], v[22:25], v[128:131], v[140:143]
	s_nop 1
	v_mfma_f32_16x16x32_f16 v[144:147], v[30:33], v[128:131], v[144:147]
	v_pk_fma_f32 v[154:155], v[106:107], v[150:151], v[108:109]
	v_pk_fma_f32 v[152:153], v[102:103], v[148:149], v[104:105]
	v_cndmask_b32_e64 v160, v136, v132, s[0:1]
	v_cndmask_b32_e64 v161, v137, v133, s[0:1]
	v_cndmask_b32_e64 v162, v138, v134, s[0:1]
	v_cndmask_b32_e64 v160, v140, v160, s[2:3]
	v_cndmask_b32_e64 v161, v141, v161, s[2:3]
	v_cndmask_b32_e64 v163, v139, v135, s[0:1]
	v_cndmask_b32_e64 v156, v160, v144, s[4:5]
	v_cndmask_b32_e64 v157, v161, v145, s[4:5]
	v_exp_f32_e32 v156, v156
	v_exp_f32_e32 v157, v157
	v_cndmask_b32_e64 v162, v142, v162, s[2:3]
	v_cndmask_b32_e64 v163, v143, v163, s[2:3]
	v_cndmask_b32_e64 v158, v162, v146, s[4:5]
	v_cndmask_b32_e64 v159, v163, v147, s[4:5]
	v_pk_add_f32 v[156:157], v[156:157], 1.0 op_sel_hi:[1,0]
	v_exp_f32_e32 v158, v158
	v_rcp_f32_e32 v156, v156
	v_rcp_f32_e32 v157, v157
	v_exp_f32_e32 v159, v159
	v_pk_fma_f32 v[148:149], v[110:111], v[156:157], v[152:153]
	v_pk_add_f32 v[158:159], v[158:159], 1.0 op_sel_hi:[1,0]
	v_cvt_pk_f16_f32 v124, v148, v149
	v_rcp_f32_e32 v158, v158
	v_rcp_f32_e32 v159, v159
	v_mov_b32_dpp v125, v124 quad_perm:[1,2,3,0] row_mask:0xf bank_mask:0xf bound_ctrl:1
	v_mov_b32_dpp v126, v124 quad_perm:[2,3,0,1] row_mask:0xf bank_mask:0xf bound_ctrl:1
	v_mov_b32_dpp v127, v124 quad_perm:[3,0,1,2] row_mask:0xf bank_mask:0xf bound_ctrl:1
	v_pk_fma_f32 v[150:151], v[112:113], v[158:159], v[154:155]
	s_waitcnt vmcnt(15)
	v_mfma_f32_16x16x32_f16 v[132:135], v[2:5], v[124:127], v[70:73]
	v_cvt_pk_f16_f32 v128, v150, v151
	s_nop 0
	v_mfma_f32_16x16x32_f16 v[136:139], v[10:13], v[124:127], v[70:73]
	v_mov_b32_dpp v129, v128 quad_perm:[1,2,3,0] row_mask:0xf bank_mask:0xf bound_ctrl:1
	v_mov_b32_dpp v130, v128 quad_perm:[2,3,0,1] row_mask:0xf bank_mask:0xf bound_ctrl:1
	v_mfma_f32_16x16x32_f16 v[140:143], v[18:21], v[124:127], v[70:73]
	v_mov_b32_dpp v131, v128 quad_perm:[3,0,1,2] row_mask:0xf bank_mask:0xf bound_ctrl:1
	ds_write_b32 v164, v124 offset:0
	v_mfma_f32_16x16x32_f16 v[144:147], v[26:29], v[124:127], v[70:73]
	global_load_dwordx4 v[70:73], v[0:1], off offset:-1792
	ds_write_b32 v164, v128 offset:4
	v_mfma_f32_16x16x32_f16 v[132:135], v[6:9], v[128:131], v[132:135]
	s_nop 1
	v_mfma_f32_16x16x32_f16 v[136:139], v[14:17], v[128:131], v[136:139]
	s_nop 1
	v_mfma_f32_16x16x32_f16 v[140:143], v[22:25], v[128:131], v[140:143]
	s_nop 1
	v_mfma_f32_16x16x32_f16 v[144:147], v[30:33], v[128:131], v[144:147]
	v_pk_fma_f32 v[154:155], v[106:107], v[150:151], v[108:109]
	v_pk_fma_f32 v[152:153], v[102:103], v[148:149], v[104:105]
	v_cndmask_b32_e64 v160, v136, v132, s[0:1]
	v_cndmask_b32_e64 v161, v137, v133, s[0:1]
	v_cndmask_b32_e64 v162, v138, v134, s[0:1]
	v_cndmask_b32_e64 v160, v140, v160, s[2:3]
	v_cndmask_b32_e64 v161, v141, v161, s[2:3]
	v_cndmask_b32_e64 v163, v139, v135, s[0:1]
	v_cndmask_b32_e64 v156, v160, v144, s[4:5]
	v_cndmask_b32_e64 v157, v161, v145, s[4:5]
	v_exp_f32_e32 v156, v156
	v_exp_f32_e32 v157, v157
	v_cndmask_b32_e64 v162, v142, v162, s[2:3]
	v_cndmask_b32_e64 v163, v143, v163, s[2:3]
	v_cndmask_b32_e64 v158, v162, v146, s[4:5]
	v_cndmask_b32_e64 v159, v163, v147, s[4:5]
	v_pk_add_f32 v[156:157], v[156:157], 1.0 op_sel_hi:[1,0]
	v_exp_f32_e32 v158, v158
	v_rcp_f32_e32 v156, v156
	v_rcp_f32_e32 v157, v157
	v_exp_f32_e32 v159, v159
	v_pk_fma_f32 v[148:149], v[110:111], v[156:157], v[152:153]
	v_pk_add_f32 v[158:159], v[158:159], 1.0 op_sel_hi:[1,0]
	v_cvt_pk_f16_f32 v124, v148, v149
	v_rcp_f32_e32 v158, v158
	v_rcp_f32_e32 v159, v159
	v_mov_b32_dpp v125, v124 quad_perm:[1,2,3,0] row_mask:0xf bank_mask:0xf bound_ctrl:1
	v_mov_b32_dpp v126, v124 quad_perm:[2,3,0,1] row_mask:0xf bank_mask:0xf bound_ctrl:1
	v_mov_b32_dpp v127, v124 quad_perm:[3,0,1,2] row_mask:0xf bank_mask:0xf bound_ctrl:1
	v_pk_fma_f32 v[150:151], v[112:113], v[158:159], v[154:155]
	s_waitcnt vmcnt(15)
	v_mfma_f32_16x16x32_f16 v[132:135], v[2:5], v[124:127], v[78:81]
	v_cvt_pk_f16_f32 v128, v150, v151
	s_nop 0
	v_mfma_f32_16x16x32_f16 v[136:139], v[10:13], v[124:127], v[78:81]
	v_mov_b32_dpp v129, v128 quad_perm:[1,2,3,0] row_mask:0xf bank_mask:0xf bound_ctrl:1
	v_mov_b32_dpp v130, v128 quad_perm:[2,3,0,1] row_mask:0xf bank_mask:0xf bound_ctrl:1
	v_mfma_f32_16x16x32_f16 v[140:143], v[18:21], v[124:127], v[78:81]
	v_mov_b32_dpp v131, v128 quad_perm:[3,0,1,2] row_mask:0xf bank_mask:0xf bound_ctrl:1
	ds_write_b32 v164, v124 offset:528
	v_mfma_f32_16x16x32_f16 v[144:147], v[26:29], v[124:127], v[78:81]
	global_load_dwordx4 v[78:81], v[0:1], off offset:-1536
	ds_write_b32 v164, v128 offset:532
	v_mfma_f32_16x16x32_f16 v[132:135], v[6:9], v[128:131], v[132:135]
	s_nop 1
	v_mfma_f32_16x16x32_f16 v[136:139], v[14:17], v[128:131], v[136:139]
	s_nop 1
	v_mfma_f32_16x16x32_f16 v[140:143], v[22:25], v[128:131], v[140:143]
	s_nop 1
	v_mfma_f32_16x16x32_f16 v[144:147], v[30:33], v[128:131], v[144:147]
	v_pk_fma_f32 v[154:155], v[106:107], v[150:151], v[108:109]
	v_pk_fma_f32 v[152:153], v[102:103], v[148:149], v[104:105]
	v_cndmask_b32_e64 v160, v136, v132, s[0:1]
	v_cndmask_b32_e64 v161, v137, v133, s[0:1]
	v_cndmask_b32_e64 v162, v138, v134, s[0:1]
	v_cndmask_b32_e64 v160, v140, v160, s[2:3]
	v_cndmask_b32_e64 v161, v141, v161, s[2:3]
	v_cndmask_b32_e64 v163, v139, v135, s[0:1]
	v_cndmask_b32_e64 v156, v160, v144, s[4:5]
	v_cndmask_b32_e64 v157, v161, v145, s[4:5]
	v_exp_f32_e32 v156, v156
	v_exp_f32_e32 v157, v157
	v_cndmask_b32_e64 v162, v142, v162, s[2:3]
	v_cndmask_b32_e64 v163, v143, v163, s[2:3]
	v_cndmask_b32_e64 v158, v162, v146, s[4:5]
	v_cndmask_b32_e64 v159, v163, v147, s[4:5]
	v_pk_add_f32 v[156:157], v[156:157], 1.0 op_sel_hi:[1,0]
	v_exp_f32_e32 v158, v158
	v_rcp_f32_e32 v156, v156
	v_rcp_f32_e32 v157, v157
	v_exp_f32_e32 v159, v159
	v_pk_fma_f32 v[148:149], v[110:111], v[156:157], v[152:153]
	v_pk_add_f32 v[158:159], v[158:159], 1.0 op_sel_hi:[1,0]
	v_cvt_pk_f16_f32 v124, v148, v149
	v_rcp_f32_e32 v158, v158
	v_rcp_f32_e32 v159, v159
	v_mov_b32_dpp v125, v124 quad_perm:[1,2,3,0] row_mask:0xf bank_mask:0xf bound_ctrl:1
	v_mov_b32_dpp v126, v124 quad_perm:[2,3,0,1] row_mask:0xf bank_mask:0xf bound_ctrl:1
	v_mov_b32_dpp v127, v124 quad_perm:[3,0,1,2] row_mask:0xf bank_mask:0xf bound_ctrl:1
	v_pk_fma_f32 v[150:151], v[112:113], v[158:159], v[154:155]
	s_waitcnt vmcnt(15)
	v_mfma_f32_16x16x32_f16 v[132:135], v[2:5], v[124:127], v[86:89]
	v_cvt_pk_f16_f32 v128, v150, v151
	s_nop 0
	v_mfma_f32_16x16x32_f16 v[136:139], v[10:13], v[124:127], v[86:89]
	v_mov_b32_dpp v129, v128 quad_perm:[1,2,3,0] row_mask:0xf bank_mask:0xf bound_ctrl:1
	v_mov_b32_dpp v130, v128 quad_perm:[2,3,0,1] row_mask:0xf bank_mask:0xf bound_ctrl:1
	v_mfma_f32_16x16x32_f16 v[140:143], v[18:21], v[124:127], v[86:89]
	v_mov_b32_dpp v131, v128 quad_perm:[3,0,1,2] row_mask:0xf bank_mask:0xf bound_ctrl:1
	ds_write_b32 v164, v124 offset:1056
	v_mfma_f32_16x16x32_f16 v[144:147], v[26:29], v[124:127], v[86:89]
	global_load_dwordx4 v[86:89], v[0:1], off offset:-1280
	ds_write_b32 v164, v128 offset:1060
	v_mfma_f32_16x16x32_f16 v[132:135], v[6:9], v[128:131], v[132:135]
	s_nop 1
	v_mfma_f32_16x16x32_f16 v[136:139], v[14:17], v[128:131], v[136:139]
	s_nop 1
	v_mfma_f32_16x16x32_f16 v[140:143], v[22:25], v[128:131], v[140:143]
	s_nop 1
	v_mfma_f32_16x16x32_f16 v[144:147], v[30:33], v[128:131], v[144:147]
	v_pk_fma_f32 v[154:155], v[106:107], v[150:151], v[108:109]
	v_pk_fma_f32 v[152:153], v[102:103], v[148:149], v[104:105]
	v_cndmask_b32_e64 v160, v136, v132, s[0:1]
	v_cndmask_b32_e64 v161, v137, v133, s[0:1]
	v_cndmask_b32_e64 v162, v138, v134, s[0:1]
	v_cndmask_b32_e64 v160, v140, v160, s[2:3]
	v_cndmask_b32_e64 v161, v141, v161, s[2:3]
	v_cndmask_b32_e64 v163, v139, v135, s[0:1]
	v_cndmask_b32_e64 v156, v160, v144, s[4:5]
	v_cndmask_b32_e64 v157, v161, v145, s[4:5]
	v_exp_f32_e32 v156, v156
	v_exp_f32_e32 v157, v157
	v_cndmask_b32_e64 v162, v142, v162, s[2:3]
	v_cndmask_b32_e64 v163, v143, v163, s[2:3]
	v_cndmask_b32_e64 v158, v162, v146, s[4:5]
	v_cndmask_b32_e64 v159, v163, v147, s[4:5]
	v_pk_add_f32 v[156:157], v[156:157], 1.0 op_sel_hi:[1,0]
	v_exp_f32_e32 v158, v158
	v_rcp_f32_e32 v156, v156
	v_rcp_f32_e32 v157, v157
	v_exp_f32_e32 v159, v159
	v_pk_fma_f32 v[148:149], v[110:111], v[156:157], v[152:153]
	v_pk_add_f32 v[158:159], v[158:159], 1.0 op_sel_hi:[1,0]
	v_cvt_pk_f16_f32 v124, v148, v149
	v_rcp_f32_e32 v158, v158
	v_rcp_f32_e32 v159, v159
	v_mov_b32_dpp v125, v124 quad_perm:[1,2,3,0] row_mask:0xf bank_mask:0xf bound_ctrl:1
	v_mov_b32_dpp v126, v124 quad_perm:[2,3,0,1] row_mask:0xf bank_mask:0xf bound_ctrl:1
	v_mov_b32_dpp v127, v124 quad_perm:[3,0,1,2] row_mask:0xf bank_mask:0xf bound_ctrl:1
	v_pk_fma_f32 v[150:151], v[112:113], v[158:159], v[154:155]
	s_waitcnt vmcnt(15)
	v_mfma_f32_16x16x32_f16 v[132:135], v[2:5], v[124:127], v[94:97]
	v_cvt_pk_f16_f32 v128, v150, v151
	s_nop 0
	v_mfma_f32_16x16x32_f16 v[136:139], v[10:13], v[124:127], v[94:97]
	v_mov_b32_dpp v129, v128 quad_perm:[1,2,3,0] row_mask:0xf bank_mask:0xf bound_ctrl:1
	v_mov_b32_dpp v130, v128 quad_perm:[2,3,0,1] row_mask:0xf bank_mask:0xf bound_ctrl:1
	v_mfma_f32_16x16x32_f16 v[140:143], v[18:21], v[124:127], v[94:97]
	v_mov_b32_dpp v131, v128 quad_perm:[3,0,1,2] row_mask:0xf bank_mask:0xf bound_ctrl:1
	ds_write_b32 v164, v124 offset:1584
	v_mfma_f32_16x16x32_f16 v[144:147], v[26:29], v[124:127], v[94:97]
	global_load_dwordx4 v[94:97], v[0:1], off offset:-1024
	ds_write_b32 v164, v128 offset:1588
	v_mfma_f32_16x16x32_f16 v[132:135], v[6:9], v[128:131], v[132:135]
	s_nop 1
	v_mfma_f32_16x16x32_f16 v[136:139], v[14:17], v[128:131], v[136:139]
	s_nop 1
	v_mfma_f32_16x16x32_f16 v[140:143], v[22:25], v[128:131], v[140:143]
	s_nop 1
	v_mfma_f32_16x16x32_f16 v[144:147], v[30:33], v[128:131], v[144:147]
	v_pk_fma_f32 v[154:155], v[106:107], v[150:151], v[108:109]
	v_pk_fma_f32 v[152:153], v[102:103], v[148:149], v[104:105]
	v_cndmask_b32_e64 v160, v136, v132, s[0:1]
	v_cndmask_b32_e64 v161, v137, v133, s[0:1]
	v_cndmask_b32_e64 v162, v138, v134, s[0:1]
	v_cndmask_b32_e64 v160, v140, v160, s[2:3]
	v_cndmask_b32_e64 v161, v141, v161, s[2:3]
	v_cndmask_b32_e64 v163, v139, v135, s[0:1]
	v_cndmask_b32_e64 v156, v160, v144, s[4:5]
	v_cndmask_b32_e64 v157, v161, v145, s[4:5]
	v_exp_f32_e32 v156, v156
	v_exp_f32_e32 v157, v157
	v_cndmask_b32_e64 v162, v142, v162, s[2:3]
	v_cndmask_b32_e64 v163, v143, v163, s[2:3]
	v_cndmask_b32_e64 v158, v162, v146, s[4:5]
	v_cndmask_b32_e64 v159, v163, v147, s[4:5]
	v_pk_add_f32 v[156:157], v[156:157], 1.0 op_sel_hi:[1,0]
	v_exp_f32_e32 v158, v158
	v_rcp_f32_e32 v156, v156
	v_rcp_f32_e32 v157, v157
	v_exp_f32_e32 v159, v159
	v_pk_fma_f32 v[148:149], v[110:111], v[156:157], v[152:153]
	v_pk_add_f32 v[158:159], v[158:159], 1.0 op_sel_hi:[1,0]
	v_cvt_pk_f16_f32 v124, v148, v149
	v_rcp_f32_e32 v158, v158
	v_rcp_f32_e32 v159, v159
	v_mov_b32_dpp v125, v124 quad_perm:[1,2,3,0] row_mask:0xf bank_mask:0xf bound_ctrl:1
	v_mov_b32_dpp v126, v124 quad_perm:[2,3,0,1] row_mask:0xf bank_mask:0xf bound_ctrl:1
	v_mov_b32_dpp v127, v124 quad_perm:[3,0,1,2] row_mask:0xf bank_mask:0xf bound_ctrl:1
	v_pk_fma_f32 v[150:151], v[112:113], v[158:159], v[154:155]
	s_waitcnt vmcnt(15)
	v_mfma_f32_16x16x32_f16 v[132:135], v[2:5], v[124:127], v[90:93]
	v_cvt_pk_f16_f32 v128, v150, v151
	s_nop 0
	v_mfma_f32_16x16x32_f16 v[136:139], v[10:13], v[124:127], v[90:93]
	v_mov_b32_dpp v129, v128 quad_perm:[1,2,3,0] row_mask:0xf bank_mask:0xf bound_ctrl:1
	v_mov_b32_dpp v130, v128 quad_perm:[2,3,0,1] row_mask:0xf bank_mask:0xf bound_ctrl:1
	v_mfma_f32_16x16x32_f16 v[140:143], v[18:21], v[124:127], v[90:93]
	v_mov_b32_dpp v131, v128 quad_perm:[3,0,1,2] row_mask:0xf bank_mask:0xf bound_ctrl:1
	ds_write_b32 v164, v124 offset:2112
	v_mfma_f32_16x16x32_f16 v[144:147], v[26:29], v[124:127], v[90:93]
	global_load_dwordx4 v[90:93], v[0:1], off offset:-768
	ds_write_b32 v164, v128 offset:2116
	v_mfma_f32_16x16x32_f16 v[132:135], v[6:9], v[128:131], v[132:135]
	s_nop 1
	v_mfma_f32_16x16x32_f16 v[136:139], v[14:17], v[128:131], v[136:139]
	s_nop 1
	v_mfma_f32_16x16x32_f16 v[140:143], v[22:25], v[128:131], v[140:143]
	s_nop 1
	v_mfma_f32_16x16x32_f16 v[144:147], v[30:33], v[128:131], v[144:147]
	v_pk_fma_f32 v[154:155], v[106:107], v[150:151], v[108:109]
	v_pk_fma_f32 v[152:153], v[102:103], v[148:149], v[104:105]
	v_cndmask_b32_e64 v160, v136, v132, s[0:1]
	v_cndmask_b32_e64 v161, v137, v133, s[0:1]
	v_cndmask_b32_e64 v162, v138, v134, s[0:1]
	v_cndmask_b32_e64 v160, v140, v160, s[2:3]
	v_cndmask_b32_e64 v161, v141, v161, s[2:3]
	v_cndmask_b32_e64 v163, v139, v135, s[0:1]
	v_cndmask_b32_e64 v156, v160, v144, s[4:5]
	v_cndmask_b32_e64 v157, v161, v145, s[4:5]
	v_exp_f32_e32 v156, v156
	v_exp_f32_e32 v157, v157
	v_cndmask_b32_e64 v162, v142, v162, s[2:3]
	v_cndmask_b32_e64 v163, v143, v163, s[2:3]
	v_cndmask_b32_e64 v158, v162, v146, s[4:5]
	v_cndmask_b32_e64 v159, v163, v147, s[4:5]
	v_pk_add_f32 v[156:157], v[156:157], 1.0 op_sel_hi:[1,0]
	v_exp_f32_e32 v158, v158
	v_rcp_f32_e32 v156, v156
	v_rcp_f32_e32 v157, v157
	v_exp_f32_e32 v159, v159
	v_pk_fma_f32 v[148:149], v[110:111], v[156:157], v[152:153]
	v_pk_add_f32 v[158:159], v[158:159], 1.0 op_sel_hi:[1,0]
	v_cvt_pk_f16_f32 v124, v148, v149
	v_rcp_f32_e32 v158, v158
	v_rcp_f32_e32 v159, v159
	v_mov_b32_dpp v125, v124 quad_perm:[1,2,3,0] row_mask:0xf bank_mask:0xf bound_ctrl:1
	v_mov_b32_dpp v126, v124 quad_perm:[2,3,0,1] row_mask:0xf bank_mask:0xf bound_ctrl:1
	v_mov_b32_dpp v127, v124 quad_perm:[3,0,1,2] row_mask:0xf bank_mask:0xf bound_ctrl:1
	v_pk_fma_f32 v[150:151], v[112:113], v[158:159], v[154:155]
	s_waitcnt vmcnt(15)
	v_mfma_f32_16x16x32_f16 v[132:135], v[2:5], v[124:127], v[82:85]
	v_cvt_pk_f16_f32 v128, v150, v151
	s_nop 0
	v_mfma_f32_16x16x32_f16 v[136:139], v[10:13], v[124:127], v[82:85]
	v_mov_b32_dpp v129, v128 quad_perm:[1,2,3,0] row_mask:0xf bank_mask:0xf bound_ctrl:1
	v_mov_b32_dpp v130, v128 quad_perm:[2,3,0,1] row_mask:0xf bank_mask:0xf bound_ctrl:1
	v_mfma_f32_16x16x32_f16 v[140:143], v[18:21], v[124:127], v[82:85]
	v_mov_b32_dpp v131, v128 quad_perm:[3,0,1,2] row_mask:0xf bank_mask:0xf bound_ctrl:1
	ds_write_b32 v164, v124 offset:2640
	v_mfma_f32_16x16x32_f16 v[144:147], v[26:29], v[124:127], v[82:85]
	global_load_dwordx4 v[82:85], v[0:1], off offset:-512
	ds_write_b32 v164, v128 offset:2644
	v_mfma_f32_16x16x32_f16 v[132:135], v[6:9], v[128:131], v[132:135]
	s_nop 1
	v_mfma_f32_16x16x32_f16 v[136:139], v[14:17], v[128:131], v[136:139]
	s_nop 1
	v_mfma_f32_16x16x32_f16 v[140:143], v[22:25], v[128:131], v[140:143]
	s_nop 1
	v_mfma_f32_16x16x32_f16 v[144:147], v[30:33], v[128:131], v[144:147]
	v_pk_fma_f32 v[154:155], v[106:107], v[150:151], v[108:109]
	v_pk_fma_f32 v[152:153], v[102:103], v[148:149], v[104:105]
	v_cndmask_b32_e64 v160, v136, v132, s[0:1]
	v_cndmask_b32_e64 v161, v137, v133, s[0:1]
	v_cndmask_b32_e64 v162, v138, v134, s[0:1]
	v_cndmask_b32_e64 v160, v140, v160, s[2:3]
	v_cndmask_b32_e64 v161, v141, v161, s[2:3]
	v_cndmask_b32_e64 v163, v139, v135, s[0:1]
	v_cndmask_b32_e64 v156, v160, v144, s[4:5]
	v_cndmask_b32_e64 v157, v161, v145, s[4:5]
	v_exp_f32_e32 v156, v156
	v_exp_f32_e32 v157, v157
	v_cndmask_b32_e64 v162, v142, v162, s[2:3]
	v_cndmask_b32_e64 v163, v143, v163, s[2:3]
	v_cndmask_b32_e64 v158, v162, v146, s[4:5]
	v_cndmask_b32_e64 v159, v163, v147, s[4:5]
	v_pk_add_f32 v[156:157], v[156:157], 1.0 op_sel_hi:[1,0]
	v_exp_f32_e32 v158, v158
	v_rcp_f32_e32 v156, v156
	v_rcp_f32_e32 v157, v157
	v_exp_f32_e32 v159, v159
	v_pk_fma_f32 v[148:149], v[110:111], v[156:157], v[152:153]
	v_pk_add_f32 v[158:159], v[158:159], 1.0 op_sel_hi:[1,0]
	v_cvt_pk_f16_f32 v124, v148, v149
	v_rcp_f32_e32 v158, v158
	v_rcp_f32_e32 v159, v159
	v_mov_b32_dpp v125, v124 quad_perm:[1,2,3,0] row_mask:0xf bank_mask:0xf bound_ctrl:1
	v_mov_b32_dpp v126, v124 quad_perm:[2,3,0,1] row_mask:0xf bank_mask:0xf bound_ctrl:1
	v_mov_b32_dpp v127, v124 quad_perm:[3,0,1,2] row_mask:0xf bank_mask:0xf bound_ctrl:1
	v_pk_fma_f32 v[150:151], v[112:113], v[158:159], v[154:155]
	s_waitcnt vmcnt(15)
	v_mfma_f32_16x16x32_f16 v[132:135], v[2:5], v[124:127], v[74:77]
	v_cvt_pk_f16_f32 v128, v150, v151
	s_nop 0
	v_mfma_f32_16x16x32_f16 v[136:139], v[10:13], v[124:127], v[74:77]
	v_mov_b32_dpp v129, v128 quad_perm:[1,2,3,0] row_mask:0xf bank_mask:0xf bound_ctrl:1
	v_mov_b32_dpp v130, v128 quad_perm:[2,3,0,1] row_mask:0xf bank_mask:0xf bound_ctrl:1
	v_mfma_f32_16x16x32_f16 v[140:143], v[18:21], v[124:127], v[74:77]
	v_mov_b32_dpp v131, v128 quad_perm:[3,0,1,2] row_mask:0xf bank_mask:0xf bound_ctrl:1
	ds_write_b32 v164, v124 offset:3168
	v_mfma_f32_16x16x32_f16 v[144:147], v[26:29], v[124:127], v[74:77]
	global_load_dwordx4 v[74:77], v[0:1], off offset:-256
	ds_write_b32 v164, v128 offset:3172
	v_mfma_f32_16x16x32_f16 v[132:135], v[6:9], v[128:131], v[132:135]
	s_nop 1
	v_mfma_f32_16x16x32_f16 v[136:139], v[14:17], v[128:131], v[136:139]
	s_nop 1
	v_mfma_f32_16x16x32_f16 v[140:143], v[22:25], v[128:131], v[140:143]
	s_nop 1
	v_mfma_f32_16x16x32_f16 v[144:147], v[30:33], v[128:131], v[144:147]
	v_pk_fma_f32 v[154:155], v[106:107], v[150:151], v[108:109]
	v_pk_fma_f32 v[152:153], v[102:103], v[148:149], v[104:105]
	v_cndmask_b32_e64 v160, v136, v132, s[0:1]
	v_cndmask_b32_e64 v161, v137, v133, s[0:1]
	v_cndmask_b32_e64 v162, v138, v134, s[0:1]
	v_cndmask_b32_e64 v160, v140, v160, s[2:3]
	v_cndmask_b32_e64 v161, v141, v161, s[2:3]
	v_cndmask_b32_e64 v163, v139, v135, s[0:1]
	v_cndmask_b32_e64 v156, v160, v144, s[4:5]
	v_cndmask_b32_e64 v157, v161, v145, s[4:5]
	v_exp_f32_e32 v156, v156
	v_exp_f32_e32 v157, v157
	v_cndmask_b32_e64 v162, v142, v162, s[2:3]
	v_cndmask_b32_e64 v163, v143, v163, s[2:3]
	v_cndmask_b32_e64 v158, v162, v146, s[4:5]
	v_cndmask_b32_e64 v159, v163, v147, s[4:5]
	v_pk_add_f32 v[156:157], v[156:157], 1.0 op_sel_hi:[1,0]
	v_exp_f32_e32 v158, v158
	v_rcp_f32_e32 v156, v156
	v_rcp_f32_e32 v157, v157
	v_exp_f32_e32 v159, v159
	v_pk_fma_f32 v[148:149], v[110:111], v[156:157], v[152:153]
	v_pk_add_f32 v[158:159], v[158:159], 1.0 op_sel_hi:[1,0]
	v_cvt_pk_f16_f32 v124, v148, v149
	v_rcp_f32_e32 v158, v158
	v_rcp_f32_e32 v159, v159
	v_mov_b32_dpp v125, v124 quad_perm:[1,2,3,0] row_mask:0xf bank_mask:0xf bound_ctrl:1
	v_mov_b32_dpp v126, v124 quad_perm:[2,3,0,1] row_mask:0xf bank_mask:0xf bound_ctrl:1
	v_mov_b32_dpp v127, v124 quad_perm:[3,0,1,2] row_mask:0xf bank_mask:0xf bound_ctrl:1
	v_pk_fma_f32 v[150:151], v[112:113], v[158:159], v[154:155]
	s_waitcnt vmcnt(15)
	v_mfma_f32_16x16x32_f16 v[132:135], v[2:5], v[124:127], v[66:69]
	v_cvt_pk_f16_f32 v128, v150, v151
	s_nop 0
	v_mfma_f32_16x16x32_f16 v[136:139], v[10:13], v[124:127], v[66:69]
	v_mov_b32_dpp v129, v128 quad_perm:[1,2,3,0] row_mask:0xf bank_mask:0xf bound_ctrl:1
	v_mov_b32_dpp v130, v128 quad_perm:[2,3,0,1] row_mask:0xf bank_mask:0xf bound_ctrl:1
	v_mfma_f32_16x16x32_f16 v[140:143], v[18:21], v[124:127], v[66:69]
	v_mov_b32_dpp v131, v128 quad_perm:[3,0,1,2] row_mask:0xf bank_mask:0xf bound_ctrl:1
	ds_write_b32 v164, v124 offset:3696
	v_mfma_f32_16x16x32_f16 v[144:147], v[26:29], v[124:127], v[66:69]
	global_load_dwordx4 v[66:69], v[0:1], off offset:0
	ds_write_b32 v164, v128 offset:3700
	v_mfma_f32_16x16x32_f16 v[132:135], v[6:9], v[128:131], v[132:135]
	s_nop 1
	v_mfma_f32_16x16x32_f16 v[136:139], v[14:17], v[128:131], v[136:139]
	s_nop 1
	v_mfma_f32_16x16x32_f16 v[140:143], v[22:25], v[128:131], v[140:143]
	s_nop 1
	v_mfma_f32_16x16x32_f16 v[144:147], v[30:33], v[128:131], v[144:147]
	v_pk_fma_f32 v[154:155], v[106:107], v[150:151], v[108:109]
	v_pk_fma_f32 v[152:153], v[102:103], v[148:149], v[104:105]
	v_cndmask_b32_e64 v160, v136, v132, s[0:1]
	v_cndmask_b32_e64 v161, v137, v133, s[0:1]
	v_cndmask_b32_e64 v162, v138, v134, s[0:1]
	v_cndmask_b32_e64 v160, v140, v160, s[2:3]
	v_cndmask_b32_e64 v161, v141, v161, s[2:3]
	v_cndmask_b32_e64 v163, v139, v135, s[0:1]
	v_cndmask_b32_e64 v156, v160, v144, s[4:5]
	v_cndmask_b32_e64 v157, v161, v145, s[4:5]
	v_exp_f32_e32 v156, v156
	v_exp_f32_e32 v157, v157
	v_cndmask_b32_e64 v162, v142, v162, s[2:3]
	v_cndmask_b32_e64 v163, v143, v163, s[2:3]
	v_cndmask_b32_e64 v158, v162, v146, s[4:5]
	v_cndmask_b32_e64 v159, v163, v147, s[4:5]
	v_pk_add_f32 v[156:157], v[156:157], 1.0 op_sel_hi:[1,0]
	v_exp_f32_e32 v158, v158
	v_rcp_f32_e32 v156, v156
	v_rcp_f32_e32 v157, v157
	v_exp_f32_e32 v159, v159
	v_pk_fma_f32 v[148:149], v[110:111], v[156:157], v[152:153]
	v_pk_add_f32 v[158:159], v[158:159], 1.0 op_sel_hi:[1,0]
	v_cvt_pk_f16_f32 v124, v148, v149
	v_rcp_f32_e32 v158, v158
	v_rcp_f32_e32 v159, v159
	v_mov_b32_dpp v125, v124 quad_perm:[1,2,3,0] row_mask:0xf bank_mask:0xf bound_ctrl:1
	v_mov_b32_dpp v126, v124 quad_perm:[2,3,0,1] row_mask:0xf bank_mask:0xf bound_ctrl:1
	v_mov_b32_dpp v127, v124 quad_perm:[3,0,1,2] row_mask:0xf bank_mask:0xf bound_ctrl:1
	v_pk_fma_f32 v[150:151], v[112:113], v[158:159], v[154:155]
	s_waitcnt vmcnt(15)
	v_mfma_f32_16x16x32_f16 v[132:135], v[2:5], v[124:127], v[58:61]
	v_cvt_pk_f16_f32 v128, v150, v151
	s_nop 0
	v_mfma_f32_16x16x32_f16 v[136:139], v[10:13], v[124:127], v[58:61]
	v_mov_b32_dpp v129, v128 quad_perm:[1,2,3,0] row_mask:0xf bank_mask:0xf bound_ctrl:1
	v_mov_b32_dpp v130, v128 quad_perm:[2,3,0,1] row_mask:0xf bank_mask:0xf bound_ctrl:1
	v_mfma_f32_16x16x32_f16 v[140:143], v[18:21], v[124:127], v[58:61]
	v_mov_b32_dpp v131, v128 quad_perm:[3,0,1,2] row_mask:0xf bank_mask:0xf bound_ctrl:1
	ds_write_b32 v164, v124 offset:4224
	v_mfma_f32_16x16x32_f16 v[144:147], v[26:29], v[124:127], v[58:61]
	global_load_dwordx4 v[58:61], v[0:1], off offset:256
	ds_write_b32 v164, v128 offset:4228
	v_mfma_f32_16x16x32_f16 v[132:135], v[6:9], v[128:131], v[132:135]
	s_nop 1
	v_mfma_f32_16x16x32_f16 v[136:139], v[14:17], v[128:131], v[136:139]
	s_nop 1
	v_mfma_f32_16x16x32_f16 v[140:143], v[22:25], v[128:131], v[140:143]
	s_nop 1
	v_mfma_f32_16x16x32_f16 v[144:147], v[30:33], v[128:131], v[144:147]
	v_pk_fma_f32 v[154:155], v[106:107], v[150:151], v[108:109]
	v_pk_fma_f32 v[152:153], v[102:103], v[148:149], v[104:105]
	v_cndmask_b32_e64 v160, v136, v132, s[0:1]
	v_cndmask_b32_e64 v161, v137, v133, s[0:1]
	v_cndmask_b32_e64 v162, v138, v134, s[0:1]
	v_cndmask_b32_e64 v160, v140, v160, s[2:3]
	v_cndmask_b32_e64 v161, v141, v161, s[2:3]
	v_cndmask_b32_e64 v163, v139, v135, s[0:1]
	v_cndmask_b32_e64 v156, v160, v144, s[4:5]
	v_cndmask_b32_e64 v157, v161, v145, s[4:5]
	v_exp_f32_e32 v156, v156
	v_exp_f32_e32 v157, v157
	v_cndmask_b32_e64 v162, v142, v162, s[2:3]
	v_cndmask_b32_e64 v163, v143, v163, s[2:3]
	v_cndmask_b32_e64 v158, v162, v146, s[4:5]
	v_cndmask_b32_e64 v159, v163, v147, s[4:5]
	v_pk_add_f32 v[156:157], v[156:157], 1.0 op_sel_hi:[1,0]
	v_exp_f32_e32 v158, v158
	v_rcp_f32_e32 v156, v156
	v_rcp_f32_e32 v157, v157
	v_exp_f32_e32 v159, v159
	v_pk_fma_f32 v[148:149], v[110:111], v[156:157], v[152:153]
	v_pk_add_f32 v[158:159], v[158:159], 1.0 op_sel_hi:[1,0]
	v_cvt_pk_f16_f32 v124, v148, v149
	v_rcp_f32_e32 v158, v158
	v_rcp_f32_e32 v159, v159
	v_mov_b32_dpp v125, v124 quad_perm:[1,2,3,0] row_mask:0xf bank_mask:0xf bound_ctrl:1
	v_mov_b32_dpp v126, v124 quad_perm:[2,3,0,1] row_mask:0xf bank_mask:0xf bound_ctrl:1
	v_mov_b32_dpp v127, v124 quad_perm:[3,0,1,2] row_mask:0xf bank_mask:0xf bound_ctrl:1
	v_pk_fma_f32 v[150:151], v[112:113], v[158:159], v[154:155]
	s_waitcnt vmcnt(15)
	v_mfma_f32_16x16x32_f16 v[132:135], v[2:5], v[124:127], v[54:57]
	v_cvt_pk_f16_f32 v128, v150, v151
	s_nop 0
	v_mfma_f32_16x16x32_f16 v[136:139], v[10:13], v[124:127], v[54:57]
	v_mov_b32_dpp v129, v128 quad_perm:[1,2,3,0] row_mask:0xf bank_mask:0xf bound_ctrl:1
	v_mov_b32_dpp v130, v128 quad_perm:[2,3,0,1] row_mask:0xf bank_mask:0xf bound_ctrl:1
	v_mfma_f32_16x16x32_f16 v[140:143], v[18:21], v[124:127], v[54:57]
	v_mov_b32_dpp v131, v128 quad_perm:[3,0,1,2] row_mask:0xf bank_mask:0xf bound_ctrl:1
	ds_write_b32 v164, v124 offset:4752
	v_mfma_f32_16x16x32_f16 v[144:147], v[26:29], v[124:127], v[54:57]
	global_load_dwordx4 v[54:57], v[0:1], off offset:512
	ds_write_b32 v164, v128 offset:4756
	v_mfma_f32_16x16x32_f16 v[132:135], v[6:9], v[128:131], v[132:135]
	s_nop 1
	v_mfma_f32_16x16x32_f16 v[136:139], v[14:17], v[128:131], v[136:139]
	s_nop 1
	v_mfma_f32_16x16x32_f16 v[140:143], v[22:25], v[128:131], v[140:143]
	s_nop 1
	v_mfma_f32_16x16x32_f16 v[144:147], v[30:33], v[128:131], v[144:147]
	v_pk_fma_f32 v[154:155], v[106:107], v[150:151], v[108:109]
	v_pk_fma_f32 v[152:153], v[102:103], v[148:149], v[104:105]
	v_cndmask_b32_e64 v160, v136, v132, s[0:1]
	v_cndmask_b32_e64 v161, v137, v133, s[0:1]
	v_cndmask_b32_e64 v162, v138, v134, s[0:1]
	v_cndmask_b32_e64 v160, v140, v160, s[2:3]
	v_cndmask_b32_e64 v161, v141, v161, s[2:3]
	v_cndmask_b32_e64 v163, v139, v135, s[0:1]
	v_cndmask_b32_e64 v156, v160, v144, s[4:5]
	v_cndmask_b32_e64 v157, v161, v145, s[4:5]
	v_exp_f32_e32 v156, v156
	v_exp_f32_e32 v157, v157
	v_cndmask_b32_e64 v162, v142, v162, s[2:3]
	v_cndmask_b32_e64 v163, v143, v163, s[2:3]
	v_cndmask_b32_e64 v158, v162, v146, s[4:5]
	v_cndmask_b32_e64 v159, v163, v147, s[4:5]
	v_pk_add_f32 v[156:157], v[156:157], 1.0 op_sel_hi:[1,0]
	v_exp_f32_e32 v158, v158
	v_rcp_f32_e32 v156, v156
	v_rcp_f32_e32 v157, v157
	v_exp_f32_e32 v159, v159
	v_pk_fma_f32 v[148:149], v[110:111], v[156:157], v[152:153]
	v_pk_add_f32 v[158:159], v[158:159], 1.0 op_sel_hi:[1,0]
	v_cvt_pk_f16_f32 v124, v148, v149
	v_rcp_f32_e32 v158, v158
	v_rcp_f32_e32 v159, v159
	v_mov_b32_dpp v125, v124 quad_perm:[1,2,3,0] row_mask:0xf bank_mask:0xf bound_ctrl:1
	v_mov_b32_dpp v126, v124 quad_perm:[2,3,0,1] row_mask:0xf bank_mask:0xf bound_ctrl:1
	v_mov_b32_dpp v127, v124 quad_perm:[3,0,1,2] row_mask:0xf bank_mask:0xf bound_ctrl:1
	v_pk_fma_f32 v[150:151], v[112:113], v[158:159], v[154:155]
	s_waitcnt vmcnt(15)
	v_mfma_f32_16x16x32_f16 v[132:135], v[2:5], v[124:127], v[50:53]
	v_cvt_pk_f16_f32 v128, v150, v151
	s_nop 0
	v_mfma_f32_16x16x32_f16 v[136:139], v[10:13], v[124:127], v[50:53]
	v_mov_b32_dpp v129, v128 quad_perm:[1,2,3,0] row_mask:0xf bank_mask:0xf bound_ctrl:1
	v_mov_b32_dpp v130, v128 quad_perm:[2,3,0,1] row_mask:0xf bank_mask:0xf bound_ctrl:1
	v_mfma_f32_16x16x32_f16 v[140:143], v[18:21], v[124:127], v[50:53]
	v_mov_b32_dpp v131, v128 quad_perm:[3,0,1,2] row_mask:0xf bank_mask:0xf bound_ctrl:1
	ds_write_b32 v164, v124 offset:5280
	v_mfma_f32_16x16x32_f16 v[144:147], v[26:29], v[124:127], v[50:53]
	global_load_dwordx4 v[50:53], v[0:1], off offset:768
	ds_write_b32 v164, v128 offset:5284
	v_mfma_f32_16x16x32_f16 v[132:135], v[6:9], v[128:131], v[132:135]
	s_nop 1
	v_mfma_f32_16x16x32_f16 v[136:139], v[14:17], v[128:131], v[136:139]
	s_nop 1
	v_mfma_f32_16x16x32_f16 v[140:143], v[22:25], v[128:131], v[140:143]
	s_nop 1
	v_mfma_f32_16x16x32_f16 v[144:147], v[30:33], v[128:131], v[144:147]
	v_pk_fma_f32 v[154:155], v[106:107], v[150:151], v[108:109]
	v_pk_fma_f32 v[152:153], v[102:103], v[148:149], v[104:105]
	v_cndmask_b32_e64 v160, v136, v132, s[0:1]
	v_cndmask_b32_e64 v161, v137, v133, s[0:1]
	v_cndmask_b32_e64 v162, v138, v134, s[0:1]
	v_cndmask_b32_e64 v160, v140, v160, s[2:3]
	v_cndmask_b32_e64 v161, v141, v161, s[2:3]
	v_cndmask_b32_e64 v163, v139, v135, s[0:1]
	v_cndmask_b32_e64 v156, v160, v144, s[4:5]
	v_cndmask_b32_e64 v157, v161, v145, s[4:5]
	v_exp_f32_e32 v156, v156
	v_exp_f32_e32 v157, v157
	v_cndmask_b32_e64 v162, v142, v162, s[2:3]
	v_cndmask_b32_e64 v163, v143, v163, s[2:3]
	v_cndmask_b32_e64 v158, v162, v146, s[4:5]
	v_cndmask_b32_e64 v159, v163, v147, s[4:5]
	v_pk_add_f32 v[156:157], v[156:157], 1.0 op_sel_hi:[1,0]
	v_exp_f32_e32 v158, v158
	v_rcp_f32_e32 v156, v156
	v_rcp_f32_e32 v157, v157
	v_exp_f32_e32 v159, v159
	v_pk_fma_f32 v[148:149], v[110:111], v[156:157], v[152:153]
	v_pk_add_f32 v[158:159], v[158:159], 1.0 op_sel_hi:[1,0]
	v_cvt_pk_f16_f32 v124, v148, v149
	v_rcp_f32_e32 v158, v158
	v_rcp_f32_e32 v159, v159
	v_mov_b32_dpp v125, v124 quad_perm:[1,2,3,0] row_mask:0xf bank_mask:0xf bound_ctrl:1
	v_mov_b32_dpp v126, v124 quad_perm:[2,3,0,1] row_mask:0xf bank_mask:0xf bound_ctrl:1
	v_mov_b32_dpp v127, v124 quad_perm:[3,0,1,2] row_mask:0xf bank_mask:0xf bound_ctrl:1
	v_pk_fma_f32 v[150:151], v[112:113], v[158:159], v[154:155]
	s_waitcnt vmcnt(15)
	v_mfma_f32_16x16x32_f16 v[132:135], v[2:5], v[124:127], v[46:49]
	v_cvt_pk_f16_f32 v128, v150, v151
	s_nop 0
	v_mfma_f32_16x16x32_f16 v[136:139], v[10:13], v[124:127], v[46:49]
	v_mov_b32_dpp v129, v128 quad_perm:[1,2,3,0] row_mask:0xf bank_mask:0xf bound_ctrl:1
	v_mov_b32_dpp v130, v128 quad_perm:[2,3,0,1] row_mask:0xf bank_mask:0xf bound_ctrl:1
	v_mfma_f32_16x16x32_f16 v[140:143], v[18:21], v[124:127], v[46:49]
	v_mov_b32_dpp v131, v128 quad_perm:[3,0,1,2] row_mask:0xf bank_mask:0xf bound_ctrl:1
	ds_write_b32 v164, v124 offset:5808
	v_mfma_f32_16x16x32_f16 v[144:147], v[26:29], v[124:127], v[46:49]
	global_load_dwordx4 v[46:49], v[0:1], off offset:1024
	ds_write_b32 v164, v128 offset:5812
	v_mfma_f32_16x16x32_f16 v[132:135], v[6:9], v[128:131], v[132:135]
	s_nop 1
	v_mfma_f32_16x16x32_f16 v[136:139], v[14:17], v[128:131], v[136:139]
	s_nop 1
	v_mfma_f32_16x16x32_f16 v[140:143], v[22:25], v[128:131], v[140:143]
	s_nop 1
	v_mfma_f32_16x16x32_f16 v[144:147], v[30:33], v[128:131], v[144:147]
	v_pk_fma_f32 v[154:155], v[106:107], v[150:151], v[108:109]
	v_pk_fma_f32 v[152:153], v[102:103], v[148:149], v[104:105]
	v_cndmask_b32_e64 v160, v136, v132, s[0:1]
	v_cndmask_b32_e64 v161, v137, v133, s[0:1]
	v_cndmask_b32_e64 v162, v138, v134, s[0:1]
	v_cndmask_b32_e64 v160, v140, v160, s[2:3]
	v_cndmask_b32_e64 v161, v141, v161, s[2:3]
	v_cndmask_b32_e64 v163, v139, v135, s[0:1]
	v_cndmask_b32_e64 v156, v160, v144, s[4:5]
	v_cndmask_b32_e64 v157, v161, v145, s[4:5]
	v_exp_f32_e32 v156, v156
	v_exp_f32_e32 v157, v157
	v_cndmask_b32_e64 v162, v142, v162, s[2:3]
	v_cndmask_b32_e64 v163, v143, v163, s[2:3]
	v_cndmask_b32_e64 v158, v162, v146, s[4:5]
	v_cndmask_b32_e64 v159, v163, v147, s[4:5]
	v_pk_add_f32 v[156:157], v[156:157], 1.0 op_sel_hi:[1,0]
	v_exp_f32_e32 v158, v158
	v_rcp_f32_e32 v156, v156
	v_rcp_f32_e32 v157, v157
	v_exp_f32_e32 v159, v159
	v_pk_fma_f32 v[148:149], v[110:111], v[156:157], v[152:153]
	v_pk_add_f32 v[158:159], v[158:159], 1.0 op_sel_hi:[1,0]
	v_cvt_pk_f16_f32 v124, v148, v149
	v_rcp_f32_e32 v158, v158
	v_rcp_f32_e32 v159, v159
	v_mov_b32_dpp v125, v124 quad_perm:[1,2,3,0] row_mask:0xf bank_mask:0xf bound_ctrl:1
	v_mov_b32_dpp v126, v124 quad_perm:[2,3,0,1] row_mask:0xf bank_mask:0xf bound_ctrl:1
	v_mov_b32_dpp v127, v124 quad_perm:[3,0,1,2] row_mask:0xf bank_mask:0xf bound_ctrl:1
	v_pk_fma_f32 v[150:151], v[112:113], v[158:159], v[154:155]
	s_waitcnt vmcnt(15)
	v_mfma_f32_16x16x32_f16 v[132:135], v[2:5], v[124:127], v[42:45]
	v_cvt_pk_f16_f32 v128, v150, v151
	s_nop 0
	v_mfma_f32_16x16x32_f16 v[136:139], v[10:13], v[124:127], v[42:45]
	v_mov_b32_dpp v129, v128 quad_perm:[1,2,3,0] row_mask:0xf bank_mask:0xf bound_ctrl:1
	v_mov_b32_dpp v130, v128 quad_perm:[2,3,0,1] row_mask:0xf bank_mask:0xf bound_ctrl:1
	v_mfma_f32_16x16x32_f16 v[140:143], v[18:21], v[124:127], v[42:45]
	v_mov_b32_dpp v131, v128 quad_perm:[3,0,1,2] row_mask:0xf bank_mask:0xf bound_ctrl:1
	ds_write_b32 v164, v124 offset:6336
	v_mfma_f32_16x16x32_f16 v[144:147], v[26:29], v[124:127], v[42:45]
	global_load_dwordx4 v[42:45], v[0:1], off offset:1280
	ds_write_b32 v164, v128 offset:6340
	v_mfma_f32_16x16x32_f16 v[132:135], v[6:9], v[128:131], v[132:135]
	s_nop 1
	v_mfma_f32_16x16x32_f16 v[136:139], v[14:17], v[128:131], v[136:139]
	s_nop 1
	v_mfma_f32_16x16x32_f16 v[140:143], v[22:25], v[128:131], v[140:143]
	s_nop 1
	v_mfma_f32_16x16x32_f16 v[144:147], v[30:33], v[128:131], v[144:147]
	v_pk_fma_f32 v[154:155], v[106:107], v[150:151], v[108:109]
	v_pk_fma_f32 v[152:153], v[102:103], v[148:149], v[104:105]
	v_cndmask_b32_e64 v160, v136, v132, s[0:1]
	v_cndmask_b32_e64 v161, v137, v133, s[0:1]
	v_cndmask_b32_e64 v162, v138, v134, s[0:1]
	v_cndmask_b32_e64 v160, v140, v160, s[2:3]
	v_cndmask_b32_e64 v161, v141, v161, s[2:3]
	v_cndmask_b32_e64 v163, v139, v135, s[0:1]
	v_cndmask_b32_e64 v156, v160, v144, s[4:5]
	v_cndmask_b32_e64 v157, v161, v145, s[4:5]
	v_exp_f32_e32 v156, v156
	v_exp_f32_e32 v157, v157
	v_cndmask_b32_e64 v162, v142, v162, s[2:3]
	v_cndmask_b32_e64 v163, v143, v163, s[2:3]
	v_cndmask_b32_e64 v158, v162, v146, s[4:5]
	v_cndmask_b32_e64 v159, v163, v147, s[4:5]
	v_pk_add_f32 v[156:157], v[156:157], 1.0 op_sel_hi:[1,0]
	v_exp_f32_e32 v158, v158
	v_rcp_f32_e32 v156, v156
	v_rcp_f32_e32 v157, v157
	v_exp_f32_e32 v159, v159
	v_pk_fma_f32 v[148:149], v[110:111], v[156:157], v[152:153]
	v_pk_add_f32 v[158:159], v[158:159], 1.0 op_sel_hi:[1,0]
	v_cvt_pk_f16_f32 v124, v148, v149
	v_rcp_f32_e32 v158, v158
	v_rcp_f32_e32 v159, v159
	v_mov_b32_dpp v125, v124 quad_perm:[1,2,3,0] row_mask:0xf bank_mask:0xf bound_ctrl:1
	v_mov_b32_dpp v126, v124 quad_perm:[2,3,0,1] row_mask:0xf bank_mask:0xf bound_ctrl:1
	v_mov_b32_dpp v127, v124 quad_perm:[3,0,1,2] row_mask:0xf bank_mask:0xf bound_ctrl:1
	v_pk_fma_f32 v[150:151], v[112:113], v[158:159], v[154:155]
	s_waitcnt vmcnt(15)
	v_mfma_f32_16x16x32_f16 v[132:135], v[2:5], v[124:127], v[38:41]
	v_cvt_pk_f16_f32 v128, v150, v151
	s_nop 0
	v_mfma_f32_16x16x32_f16 v[136:139], v[10:13], v[124:127], v[38:41]
	v_mov_b32_dpp v129, v128 quad_perm:[1,2,3,0] row_mask:0xf bank_mask:0xf bound_ctrl:1
	v_mov_b32_dpp v130, v128 quad_perm:[2,3,0,1] row_mask:0xf bank_mask:0xf bound_ctrl:1
	v_mfma_f32_16x16x32_f16 v[140:143], v[18:21], v[124:127], v[38:41]
	v_mov_b32_dpp v131, v128 quad_perm:[3,0,1,2] row_mask:0xf bank_mask:0xf bound_ctrl:1
	ds_write_b32 v164, v124 offset:6864
	v_mfma_f32_16x16x32_f16 v[144:147], v[26:29], v[124:127], v[38:41]
	global_load_dwordx4 v[38:41], v[0:1], off offset:1536
	ds_write_b32 v164, v128 offset:6868
	v_mfma_f32_16x16x32_f16 v[132:135], v[6:9], v[128:131], v[132:135]
	s_nop 1
	v_mfma_f32_16x16x32_f16 v[136:139], v[14:17], v[128:131], v[136:139]
	s_nop 1
	v_mfma_f32_16x16x32_f16 v[140:143], v[22:25], v[128:131], v[140:143]
	s_nop 1
	v_mfma_f32_16x16x32_f16 v[144:147], v[30:33], v[128:131], v[144:147]
	v_pk_fma_f32 v[154:155], v[106:107], v[150:151], v[108:109]
	v_pk_fma_f32 v[152:153], v[102:103], v[148:149], v[104:105]
	v_cndmask_b32_e64 v160, v136, v132, s[0:1]
	v_cndmask_b32_e64 v161, v137, v133, s[0:1]
	v_cndmask_b32_e64 v162, v138, v134, s[0:1]
	v_cndmask_b32_e64 v160, v140, v160, s[2:3]
	v_cndmask_b32_e64 v161, v141, v161, s[2:3]
	v_cndmask_b32_e64 v163, v139, v135, s[0:1]
	v_cndmask_b32_e64 v156, v160, v144, s[4:5]
	v_cndmask_b32_e64 v157, v161, v145, s[4:5]
	v_exp_f32_e32 v156, v156
	v_exp_f32_e32 v157, v157
	v_cndmask_b32_e64 v162, v142, v162, s[2:3]
	v_cndmask_b32_e64 v163, v143, v163, s[2:3]
	v_cndmask_b32_e64 v158, v162, v146, s[4:5]
	v_cndmask_b32_e64 v159, v163, v147, s[4:5]
	v_pk_add_f32 v[156:157], v[156:157], 1.0 op_sel_hi:[1,0]
	v_exp_f32_e32 v158, v158
	v_rcp_f32_e32 v156, v156
	v_rcp_f32_e32 v157, v157
	v_exp_f32_e32 v159, v159
	v_pk_fma_f32 v[148:149], v[110:111], v[156:157], v[152:153]
	v_pk_add_f32 v[158:159], v[158:159], 1.0 op_sel_hi:[1,0]
	v_cvt_pk_f16_f32 v124, v148, v149
	v_rcp_f32_e32 v158, v158
	v_rcp_f32_e32 v159, v159
	v_mov_b32_dpp v125, v124 quad_perm:[1,2,3,0] row_mask:0xf bank_mask:0xf bound_ctrl:1
	v_mov_b32_dpp v126, v124 quad_perm:[2,3,0,1] row_mask:0xf bank_mask:0xf bound_ctrl:1
	v_mov_b32_dpp v127, v124 quad_perm:[3,0,1,2] row_mask:0xf bank_mask:0xf bound_ctrl:1
	v_pk_fma_f32 v[150:151], v[112:113], v[158:159], v[154:155]
	s_waitcnt vmcnt(15)
	v_mfma_f32_16x16x32_f16 v[132:135], v[2:5], v[124:127], v[34:37]
	v_cvt_pk_f16_f32 v128, v150, v151
	s_nop 0
	v_mfma_f32_16x16x32_f16 v[136:139], v[10:13], v[124:127], v[34:37]
	v_mov_b32_dpp v129, v128 quad_perm:[1,2,3,0] row_mask:0xf bank_mask:0xf bound_ctrl:1
	v_mov_b32_dpp v130, v128 quad_perm:[2,3,0,1] row_mask:0xf bank_mask:0xf bound_ctrl:1
	v_mfma_f32_16x16x32_f16 v[140:143], v[18:21], v[124:127], v[34:37]
	v_mov_b32_dpp v131, v128 quad_perm:[3,0,1,2] row_mask:0xf bank_mask:0xf bound_ctrl:1
	ds_write_b32 v164, v124 offset:7392
	v_mfma_f32_16x16x32_f16 v[144:147], v[26:29], v[124:127], v[34:37]
	global_load_dwordx4 v[34:37], v[0:1], off offset:1792
	ds_write_b32 v164, v128 offset:7396
	v_mfma_f32_16x16x32_f16 v[132:135], v[6:9], v[128:131], v[132:135]
	s_nop 1
	v_mfma_f32_16x16x32_f16 v[136:139], v[14:17], v[128:131], v[136:139]
	s_nop 1
	v_mfma_f32_16x16x32_f16 v[140:143], v[22:25], v[128:131], v[140:143]
	s_nop 1
	v_mfma_f32_16x16x32_f16 v[144:147], v[30:33], v[128:131], v[144:147]
	v_pk_fma_f32 v[154:155], v[106:107], v[150:151], v[108:109]
	v_pk_fma_f32 v[152:153], v[102:103], v[148:149], v[104:105]
	v_cndmask_b32_e64 v160, v136, v132, s[0:1]
	v_cndmask_b32_e64 v161, v137, v133, s[0:1]
	v_cndmask_b32_e64 v162, v138, v134, s[0:1]
	v_cndmask_b32_e64 v160, v140, v160, s[2:3]
	v_cndmask_b32_e64 v161, v141, v161, s[2:3]
	v_cndmask_b32_e64 v163, v139, v135, s[0:1]
	v_cndmask_b32_e64 v156, v160, v144, s[4:5]
	v_cndmask_b32_e64 v157, v161, v145, s[4:5]
	v_exp_f32_e32 v156, v156
	v_exp_f32_e32 v157, v157
	v_cndmask_b32_e64 v162, v142, v162, s[2:3]
	v_cndmask_b32_e64 v163, v143, v163, s[2:3]
	v_cndmask_b32_e64 v158, v162, v146, s[4:5]
	v_cndmask_b32_e64 v159, v163, v147, s[4:5]
	v_pk_add_f32 v[156:157], v[156:157], 1.0 op_sel_hi:[1,0]
	v_exp_f32_e32 v158, v158
	v_rcp_f32_e32 v156, v156
	v_rcp_f32_e32 v157, v157
	v_exp_f32_e32 v159, v159
	v_pk_fma_f32 v[148:149], v[110:111], v[156:157], v[152:153]
	v_pk_add_f32 v[158:159], v[158:159], 1.0 op_sel_hi:[1,0]
	v_cvt_pk_f16_f32 v124, v148, v149
	v_rcp_f32_e32 v158, v158
	v_rcp_f32_e32 v159, v159
	v_mov_b32_dpp v125, v124 quad_perm:[1,2,3,0] row_mask:0xf bank_mask:0xf bound_ctrl:1
	v_mov_b32_dpp v126, v124 quad_perm:[2,3,0,1] row_mask:0xf bank_mask:0xf bound_ctrl:1
	v_mov_b32_dpp v127, v124 quad_perm:[3,0,1,2] row_mask:0xf bank_mask:0xf bound_ctrl:1
	v_pk_fma_f32 v[150:151], v[112:113], v[158:159], v[154:155]
	s_nop 0
	v_cvt_pk_f16_f32 v128, v150, v151
	ds_write_b32 v164, v124 offset:7920
	s_nop 0
	v_mov_b32_dpp v129, v128 quad_perm:[1,2,3,0] row_mask:0xf bank_mask:0xf bound_ctrl:1
	v_mov_b32_dpp v130, v128 quad_perm:[2,3,0,1] row_mask:0xf bank_mask:0xf bound_ctrl:1
	v_mov_b32_dpp v131, v128 quad_perm:[3,0,1,2] row_mask:0xf bank_mask:0xf bound_ctrl:1
	ds_write_b32 v164, v128 offset:7924
	s_branch .LBB3_168
